# speedup vs baseline: 1.0007x; 1.0007x over previous
.LBB1_66:
	s_or_b64 exec, exec, s[28:29]
	s_add_i32 s25, 0, 0x18000
	v_add_u32_e32 v220, s25, v222
	s_mov_b64 s[28:29], 0x80
	v_readfirstlane_b32 s30, v220
	v_add_u32_e32 v151, 0x2000, v220
	v_lshl_add_u64 v[2:3], v[2:3], 0, s[28:29]
	s_mov_b32 m0, s30
	v_readfirstlane_b32 s30, v151
	v_add_u32_e32 v152, 0x8000, v218
	s_waitcnt vmcnt(4)
	s_barrier
	global_load_lds_dwordx4 v[2:3], off
	v_lshl_add_u64 v[2:3], v[4:5], 0, s[28:29]
	s_mov_b32 m0, s30
	v_readfirstlane_b32 s30, v152
	v_add_u32_e32 v153, 0xa000, v218
	global_load_lds_dwordx4 v[2:3], off
	v_lshl_add_u64 v[2:3], v[6:7], 0, s[28:29]
	s_mov_b32 m0, s30
	v_readfirstlane_b32 s30, v153
	global_load_lds_dwordx4 v[2:3], off
	s_mov_b32 m0, s30
	s_add_i32 s30, 0, 0x1c000
	v_add_u32_e32 v221, s30, v222
	v_lshl_add_u64 v[2:3], v[8:9], 0, s[28:29]
	v_readfirstlane_b32 s31, v221
	global_load_lds_dwordx4 v[2:3], off
	v_lshl_add_u64 v[2:3], v[10:11], 0, s[28:29]
	s_mov_b32 m0, s31
	v_add_u32_e32 v154, 0x2000, v221
	global_load_lds_dwordx4 v[2:3], off
	v_lshl_add_u64 v[2:3], v[12:13], 0, s[28:29]
	v_readfirstlane_b32 s28, v154
	s_mov_b32 m0, s28
	v_lshlrev_b32_e32 v4, 6, v0
	global_load_lds_dwordx4 v[2:3], off
	v_lshlrev_b32_e32 v5, 2, v0
	v_and_b32_e32 v3, 48, v0
	v_and_b32_e32 v4, 0x3c0, v4
	v_and_b32_e32 v5, 32, v5
	v_bitop3_b32 v225, v4, v5, v3 bitop3:0x36
	v_add_u32_e32 v3, s3, v225
	v_lshrrev_b32_e32 v217, 7, v0
	v_lshlrev_b32_e32 v10, 12, v14
	s_add_u32 s0, s14, s0
	v_lshlrev_b32_e32 v11, 5, v17
	s_mov_b32 s3, 0x70000
	v_lshl_or_b32 v208, v217, 16, v10
	v_mov_b32_e32 v209, v205
	s_addc_u32 s1, s15, s1
	v_and_or_b32 v210, v11, s3, v10
	v_mov_b32_e32 v211, v205
	v_bfe_u32 v226, v0, 6, 2
	s_waitcnt vmcnt(6)
	v_lshlrev_b32_e32 v6, 13, v18
	v_lshl_add_u64 v[134:135], s[0:1], 0, v[208:209]
	v_lshl_add_u64 v[136:137], s[0:1], 0, v[210:211]
	s_add_u32 s0, s12, s26
	v_lshlrev_b32_e32 v2, 12, v226
	v_add_u32_e32 v223, s23, v225
	v_add_u32_e32 v4, s25, v225
	v_add_u32_e32 v5, s30, v225
	v_add_u32_e32 v224, 0, v225
	v_or_b32_e32 v7, 0x800, v6
	v_or_b32_e32 v8, 0x1000, v6
	v_or_b32_e32 v9, 0x1800, v6
	s_addc_u32 s1, s13, s27
	v_and_b32_e32 v1, 15, v0
	v_lshlrev_b32_e32 v214, 6, v18
	v_add_u32_e32 v202, v15, v16
	v_mov_b32_e32 v203, v205
	v_lshl_add_u64 v[138:139], s[0:1], 0, v[208:209]
	v_lshl_add_u64 v[140:141], s[0:1], 0, v[210:211]
	s_mov_b32 s3, -2
	s_mov_b64 s[0:1], 0x80080
	s_mov_b64 s[26:27], 0x100
	s_mov_b64 s[28:29], 0x80100
	s_mov_b64 s[30:31], 0x180
	s_mov_b64 s[34:35], 0x80180
	v_add_u32_e32 v156, v3, v2
	v_add_u32_e32 v145, v224, v6
	v_add_u32_e32 v144, v224, v7
	v_add_u32_e32 v143, v224, v8
	v_add_u32_e32 v142, v224, v9
	v_add_u32_e32 v155, v223, v2
	v_add_u32_e32 v148, v4, v2
	v_add_u32_e32 v146, v5, v2
	v_mov_b32_e32 v2, v205
	v_mov_b32_e32 v3, v205
	v_mov_b32_e32 v4, v205
	v_mov_b32_e32 v5, v205
	v_mov_b32_e32 v6, v205
	v_mov_b32_e32 v7, v205
	v_mov_b32_e32 v8, v205
	v_mov_b32_e32 v9, v205
	v_mov_b32_e32 v10, v205
	v_mov_b32_e32 v11, v205
	v_mov_b32_e32 v12, v205
	v_mov_b32_e32 v13, v205
	v_mov_b32_e32 v14, v205
	v_mov_b32_e32 v15, v205
	v_mov_b32_e32 v16, v205
	v_mov_b32_e32 v17, v205
	v_mov_b32_e32 v18, v205
	v_mov_b32_e32 v19, v205
	v_mov_b32_e32 v20, v205
	v_mov_b32_e32 v21, v205
	v_mov_b32_e32 v22, v205
	v_mov_b32_e32 v23, v205
	v_mov_b32_e32 v24, v205
	v_mov_b32_e32 v25, v205
	v_mov_b32_e32 v26, v205
	v_mov_b32_e32 v27, v205
	v_mov_b32_e32 v28, v205
	v_mov_b32_e32 v29, v205
	v_mov_b32_e32 v30, v205
	v_mov_b32_e32 v31, v205
	v_mov_b32_e32 v32, v205
	v_mov_b32_e32 v33, v205
	v_mov_b32_e32 v34, v205
	v_mov_b32_e32 v35, v205
	v_mov_b32_e32 v36, v205
	v_mov_b32_e32 v37, v205
	v_mov_b32_e32 v38, v205
	v_mov_b32_e32 v39, v205
	v_mov_b32_e32 v40, v205
	v_mov_b32_e32 v41, v205
	v_mov_b32_e32 v42, v205
	v_mov_b32_e32 v43, v205
	v_mov_b32_e32 v44, v205
	v_mov_b32_e32 v45, v205
	v_mov_b32_e32 v46, v205
	v_mov_b32_e32 v47, v205
	v_mov_b32_e32 v48, v205
	v_mov_b32_e32 v49, v205
	v_mov_b32_e32 v50, v205
	v_mov_b32_e32 v51, v205
	v_mov_b32_e32 v52, v205
	v_mov_b32_e32 v53, v205
	v_mov_b32_e32 v54, v205
	v_mov_b32_e32 v55, v205
	v_mov_b32_e32 v56, v205
	v_mov_b32_e32 v57, v205
	v_mov_b32_e32 v58, v205
	v_mov_b32_e32 v59, v205
	v_mov_b32_e32 v60, v205
	v_mov_b32_e32 v61, v205
	v_mov_b32_e32 v62, v205
	v_mov_b32_e32 v63, v205
	v_mov_b32_e32 v64, v205
	v_mov_b32_e32 v65, v205
	v_mov_b32_e32 v66, v205
	v_mov_b32_e32 v67, v205
	v_mov_b32_e32 v68, v205
	v_mov_b32_e32 v69, v205
	v_mov_b32_e32 v74, v205
	v_mov_b32_e32 v75, v205
	v_mov_b32_e32 v76, v205
	v_mov_b32_e32 v77, v205
	v_mov_b32_e32 v82, v205
	v_mov_b32_e32 v83, v205
	v_mov_b32_e32 v84, v205
	v_mov_b32_e32 v85, v205
	v_mov_b32_e32 v86, v205
	v_mov_b32_e32 v87, v205
	v_mov_b32_e32 v88, v205
	v_mov_b32_e32 v89, v205
	v_mov_b32_e32 v90, v205
	v_mov_b32_e32 v91, v205
	v_mov_b32_e32 v92, v205
	v_mov_b32_e32 v93, v205
	v_mov_b32_e32 v94, v205
	v_mov_b32_e32 v95, v205
	v_mov_b32_e32 v96, v205
	v_mov_b32_e32 v97, v205
	v_mov_b32_e32 v98, v205
	v_mov_b32_e32 v99, v205
	v_mov_b32_e32 v100, v205
	v_mov_b32_e32 v101, v205
	v_mov_b32_e32 v102, v205
	v_mov_b32_e32 v103, v205
	v_mov_b32_e32 v104, v205
	v_mov_b32_e32 v105, v205
	v_mov_b32_e32 v106, v205
	v_mov_b32_e32 v107, v205
	v_mov_b32_e32 v108, v205
	v_mov_b32_e32 v109, v205
	v_mov_b32_e32 v110, v205
	v_mov_b32_e32 v111, v205
	v_mov_b32_e32 v112, v205
	v_mov_b32_e32 v113, v205
	v_mov_b32_e32 v114, v205
	v_mov_b32_e32 v115, v205
	v_mov_b32_e32 v116, v205
	v_mov_b32_e32 v117, v205
	v_mov_b32_e32 v118, v205
	v_mov_b32_e32 v119, v205
	v_mov_b32_e32 v120, v205
	v_mov_b32_e32 v121, v205
	v_mov_b32_e32 v122, v205
	v_mov_b32_e32 v123, v205
	v_mov_b32_e32 v124, v205
	v_mov_b32_e32 v125, v205
	v_mov_b32_e32 v126, v205
	v_mov_b32_e32 v127, v205
	v_mov_b32_e32 v128, v205
	v_mov_b32_e32 v129, v205
	v_mov_b32_e32 v70, v205
	v_mov_b32_e32 v71, v205
	v_mov_b32_e32 v72, v205
	v_mov_b32_e32 v73, v205
	v_mov_b32_e32 v78, v205
	v_mov_b32_e32 v79, v205
	v_mov_b32_e32 v80, v205
	v_mov_b32_e32 v81, v205
	s_barrier
	s_nop 1
	v_readfirstlane_b32 s74, v216
	v_readfirstlane_b32 s75, v218
	v_readfirstlane_b32 s76, v147
	v_readfirstlane_b32 s77, v219
	v_readfirstlane_b32 s78, v149
	v_readfirstlane_b32 s79, v150
	v_readfirstlane_b32 s80, v220
	v_readfirstlane_b32 s81, v151
	v_readfirstlane_b32 s82, v152
	v_readfirstlane_b32 s83, v153
	v_readfirstlane_b32 s84, v221
	v_readfirstlane_b32 s85, v154
	v_add_u32_e32 v157, 0xc000, v218
	s_nop 0
	v_readfirstlane_b32 s86, v157
	v_add_u32_e32 v157, 0xe000, v218
	s_nop 0
	v_readfirstlane_b32 s87, v157
	v_add_u32_e32 v157, 0x2000, v216
	s_nop 0
	v_readfirstlane_b32 s88, v157
	v_add_u32_e32 v157, 0x2000, v219
	s_nop 0
	v_readfirstlane_b32 s89, v157
.LBB1_67:
	ds_read_b128 v[158:161], v156
	ds_read_b128 v[162:165], v156 offset:1024
	ds_read_b128 v[166:169], v156 offset:2048
	ds_read_b128 v[170:173], v156 offset:3072
	v_lshl_add_u64 v[212:213], v[138:139], 0, v[202:203]
	v_lshl_add_u64 v[174:175], v[212:213], 0, s[0:1]
	s_mov_b32 m0, s86
	v_lshl_add_u64 v[250:251], v[140:141], 0, v[202:203]
	global_load_lds_dwordx4 v[174:175], off
	s_mov_b32 m0, s87
	v_lshl_add_u64 v[174:175], v[250:251], 0, s[0:1]
	global_load_lds_dwordx4 v[174:175], off
	ds_read_b128 v[174:177], v145
	ds_read_b128 v[178:181], v145 offset:1024
	ds_read_b128 v[182:185], v144
	ds_read_b128 v[186:189], v144 offset:1024
	ds_read_b128 v[190:193], v143
	ds_read_b128 v[194:197], v143 offset:1024
	ds_read_b128 v[198:201], v142
	ds_read_b128 v[230:233], v142 offset:1024
	s_waitcnt lgkmcnt(8)
	s_barrier
	s_waitcnt lgkmcnt(0)
	s_setprio 1
	s_waitcnt lgkmcnt(0)
	v_mfma_f32_16x16x32_f16 v[126:129], v[158:161], v[174:177], v[126:129]
	v_mfma_f32_16x16x32_f16 v[122:125], v[166:169], v[174:177], v[122:125]
	v_mfma_f32_16x16x32_f16 v[118:121], v[158:161], v[182:185], v[118:121]
	v_mfma_f32_16x16x32_f16 v[114:117], v[166:169], v[182:185], v[114:117]
	v_mfma_f32_16x16x32_f16 v[110:113], v[158:161], v[190:193], v[110:113]
	v_mfma_f32_16x16x32_f16 v[106:109], v[166:169], v[190:193], v[106:109]
	v_mfma_f32_16x16x32_f16 v[102:105], v[158:161], v[198:201], v[102:105]
	v_mfma_f32_16x16x32_f16 v[98:101], v[166:169], v[198:201], v[98:101]
	v_mfma_f32_16x16x32_f16 v[126:129], v[162:165], v[178:181], v[126:129]
	v_mfma_f32_16x16x32_f16 v[122:125], v[170:173], v[178:181], v[122:125]
	v_mfma_f32_16x16x32_f16 v[118:121], v[162:165], v[186:189], v[118:121]
	v_mfma_f32_16x16x32_f16 v[114:117], v[170:173], v[186:189], v[114:117]
	v_mfma_f32_16x16x32_f16 v[110:113], v[162:165], v[194:197], v[110:113]
	v_mfma_f32_16x16x32_f16 v[106:109], v[170:173], v[194:197], v[106:109]
	v_mfma_f32_16x16x32_f16 v[102:105], v[162:165], v[230:233], v[102:105]
	v_mfma_f32_16x16x32_f16 v[98:101], v[170:173], v[230:233], v[98:101]
	s_setprio 0
	s_barrier
	v_lshl_add_u64 v[252:253], v[134:135], 0, v[202:203]
	v_lshl_add_u64 v[254:255], v[252:253], 0, s[26:27]
	s_mov_b32 m0, s74
	ds_read_b128 v[234:237], v155
	ds_read_b128 v[238:241], v155 offset:1024
	ds_read_b128 v[242:245], v155 offset:2048
	ds_read_b128 v[246:249], v155 offset:3072
	global_load_lds_dwordx4 v[254:255], off
	v_lshl_add_u64 v[254:255], v[136:137], 0, v[202:203]
	s_mov_b32 m0, s88
	v_lshl_add_u64 v[228:229], v[254:255], 0, s[26:27]
	global_load_lds_dwordx4 v[228:229], off
	s_barrier
	s_waitcnt lgkmcnt(0)
	s_setprio 1
	s_waitcnt lgkmcnt(0)
	v_mfma_f32_16x16x32_f16 v[94:97], v[234:237], v[174:177], v[94:97]
	v_mfma_f32_16x16x32_f16 v[90:93], v[242:245], v[174:177], v[90:93]
	v_mfma_f32_16x16x32_f16 v[86:89], v[234:237], v[182:185], v[86:89]
	v_mfma_f32_16x16x32_f16 v[82:85], v[242:245], v[182:185], v[82:85]
	v_mfma_f32_16x16x32_f16 v[74:77], v[234:237], v[190:193], v[74:77]
	v_mfma_f32_16x16x32_f16 v[66:69], v[242:245], v[190:193], v[66:69]
	v_mfma_f32_16x16x32_f16 v[62:65], v[234:237], v[198:201], v[62:65]
	v_mfma_f32_16x16x32_f16 v[58:61], v[242:245], v[198:201], v[58:61]
	v_mfma_f32_16x16x32_f16 v[94:97], v[238:241], v[178:181], v[94:97]
	v_mfma_f32_16x16x32_f16 v[90:93], v[246:249], v[178:181], v[90:93]
	v_mfma_f32_16x16x32_f16 v[86:89], v[238:241], v[186:189], v[86:89]
	v_mfma_f32_16x16x32_f16 v[82:85], v[246:249], v[186:189], v[82:85]
	v_mfma_f32_16x16x32_f16 v[74:77], v[238:241], v[194:197], v[74:77]
	v_mfma_f32_16x16x32_f16 v[66:69], v[246:249], v[194:197], v[66:69]
	v_mfma_f32_16x16x32_f16 v[62:65], v[238:241], v[230:233], v[62:65]
	v_mfma_f32_16x16x32_f16 v[58:61], v[246:249], v[230:233], v[58:61]
	s_setprio 0
	v_lshl_add_u64 v[228:229], v[212:213], 0, s[26:27]
	s_mov_b32 m0, s75
	s_barrier
	ds_read_b128 v[174:177], v145 offset:16384
	ds_read_b128 v[178:181], v145 offset:17408
	ds_read_b128 v[182:185], v144 offset:16384
	ds_read_b128 v[186:189], v144 offset:17408
	ds_read_b128 v[190:193], v143 offset:16384
	ds_read_b128 v[194:197], v143 offset:17408
	ds_read_b128 v[198:201], v142 offset:16384
	ds_read_b128 v[230:233], v142 offset:17408
	global_load_lds_dwordx4 v[228:229], off
	s_mov_b32 m0, s76
	v_lshl_add_u64 v[228:229], v[250:251], 0, s[26:27]
	global_load_lds_dwordx4 v[228:229], off
	s_barrier
	s_waitcnt lgkmcnt(0)
	s_setprio 1
	s_waitcnt lgkmcnt(0)
	v_mfma_f32_16x16x32_f16 v[54:57], v[158:161], v[174:177], v[54:57]
	v_mfma_f32_16x16x32_f16 v[50:53], v[166:169], v[174:177], v[50:53]
	v_mfma_f32_16x16x32_f16 v[46:49], v[158:161], v[182:185], v[46:49]
	v_mfma_f32_16x16x32_f16 v[42:45], v[166:169], v[182:185], v[42:45]
	v_mfma_f32_16x16x32_f16 v[38:41], v[158:161], v[190:193], v[38:41]
	v_mfma_f32_16x16x32_f16 v[34:37], v[166:169], v[190:193], v[34:37]
	v_mfma_f32_16x16x32_f16 v[30:33], v[158:161], v[198:201], v[30:33]
	v_mfma_f32_16x16x32_f16 v[26:29], v[166:169], v[198:201], v[26:29]
	v_mfma_f32_16x16x32_f16 v[54:57], v[162:165], v[178:181], v[54:57]
	v_mfma_f32_16x16x32_f16 v[50:53], v[170:173], v[178:181], v[50:53]
	v_mfma_f32_16x16x32_f16 v[46:49], v[162:165], v[186:189], v[46:49]
	v_mfma_f32_16x16x32_f16 v[42:45], v[170:173], v[186:189], v[42:45]
	v_mfma_f32_16x16x32_f16 v[38:41], v[162:165], v[194:197], v[38:41]
	v_mfma_f32_16x16x32_f16 v[34:37], v[170:173], v[194:197], v[34:37]
	v_mfma_f32_16x16x32_f16 v[30:33], v[162:165], v[230:233], v[30:33]
	v_mfma_f32_16x16x32_f16 v[26:29], v[170:173], v[230:233], v[26:29]
	s_setprio 0
	s_barrier
	v_lshl_add_u64 v[158:159], v[252:253], 0, s[28:29]
	s_mov_b32 m0, s77
	s_nop 0
	global_load_lds_dwordx4 v[158:159], off
	s_mov_b32 m0, s89
	v_lshl_add_u64 v[158:159], v[254:255], 0, s[28:29]
	global_load_lds_dwordx4 v[158:159], off
	s_waitcnt vmcnt(6)
	s_barrier
	s_setprio 1
	v_mfma_f32_16x16x32_f16 v[22:25], v[234:237], v[174:177], v[22:25]
	v_mfma_f32_16x16x32_f16 v[18:21], v[242:245], v[174:177], v[18:21]
	v_mfma_f32_16x16x32_f16 v[14:17], v[234:237], v[182:185], v[14:17]
	v_mfma_f32_16x16x32_f16 v[10:13], v[242:245], v[182:185], v[10:13]
	v_mfma_f32_16x16x32_f16 v[6:9], v[234:237], v[190:193], v[6:9]
	v_mfma_f32_16x16x32_f16 v[2:5], v[242:245], v[190:193], v[2:5]
	v_mfma_f32_16x16x32_f16 v[70:73], v[234:237], v[198:201], v[70:73]
	v_mfma_f32_16x16x32_f16 v[78:81], v[242:245], v[198:201], v[78:81]
	v_mfma_f32_16x16x32_f16 v[22:25], v[238:241], v[178:181], v[22:25]
	v_mfma_f32_16x16x32_f16 v[18:21], v[246:249], v[178:181], v[18:21]
	v_mfma_f32_16x16x32_f16 v[14:17], v[238:241], v[186:189], v[14:17]
	v_mfma_f32_16x16x32_f16 v[10:13], v[246:249], v[186:189], v[10:13]
	v_mfma_f32_16x16x32_f16 v[6:9], v[238:241], v[194:197], v[6:9]
	v_mfma_f32_16x16x32_f16 v[2:5], v[246:249], v[194:197], v[2:5]
	v_mfma_f32_16x16x32_f16 v[70:73], v[238:241], v[230:233], v[70:73]
	v_mfma_f32_16x16x32_f16 v[78:81], v[246:249], v[230:233], v[78:81]
	s_setprio 0
	s_barrier
	ds_read_b128 v[158:161], v148
	ds_read_b128 v[162:165], v148 offset:1024
	ds_read_b128 v[166:169], v148 offset:2048
	ds_read_b128 v[170:173], v148 offset:3072
	v_lshl_add_u64 v[228:229], v[212:213], 0, s[28:29]
	s_mov_b32 m0, s78
	ds_read_b128 v[174:177], v145 offset:32768
	ds_read_b128 v[178:181], v145 offset:33792
	ds_read_b128 v[182:185], v144 offset:32768
	ds_read_b128 v[186:189], v144 offset:33792
	ds_read_b128 v[190:193], v143 offset:32768
	ds_read_b128 v[194:197], v143 offset:33792
	ds_read_b128 v[198:201], v142 offset:32768
	ds_read_b128 v[230:233], v142 offset:33792
	global_load_lds_dwordx4 v[228:229], off
	s_mov_b32 m0, s79
	v_lshl_add_u64 v[228:229], v[250:251], 0, s[28:29]
	global_load_lds_dwordx4 v[228:229], off
	s_waitcnt lgkmcnt(8)
	s_barrier
	s_waitcnt lgkmcnt(0)
	s_setprio 1
	s_waitcnt lgkmcnt(0)
	v_mfma_f32_16x16x32_f16 v[126:129], v[158:161], v[174:177], v[126:129]
	v_mfma_f32_16x16x32_f16 v[122:125], v[166:169], v[174:177], v[122:125]
	v_mfma_f32_16x16x32_f16 v[118:121], v[158:161], v[182:185], v[118:121]
	v_mfma_f32_16x16x32_f16 v[114:117], v[166:169], v[182:185], v[114:117]
	v_mfma_f32_16x16x32_f16 v[110:113], v[158:161], v[190:193], v[110:113]
	v_mfma_f32_16x16x32_f16 v[106:109], v[166:169], v[190:193], v[106:109]
	v_mfma_f32_16x16x32_f16 v[102:105], v[158:161], v[198:201], v[102:105]
	v_mfma_f32_16x16x32_f16 v[98:101], v[166:169], v[198:201], v[98:101]
	v_mfma_f32_16x16x32_f16 v[126:129], v[162:165], v[178:181], v[126:129]
	v_mfma_f32_16x16x32_f16 v[122:125], v[170:173], v[178:181], v[122:125]
	v_mfma_f32_16x16x32_f16 v[118:121], v[162:165], v[186:189], v[118:121]
	v_mfma_f32_16x16x32_f16 v[114:117], v[170:173], v[186:189], v[114:117]
	v_mfma_f32_16x16x32_f16 v[110:113], v[162:165], v[194:197], v[110:113]
	v_mfma_f32_16x16x32_f16 v[106:109], v[170:173], v[194:197], v[106:109]
	v_mfma_f32_16x16x32_f16 v[102:105], v[162:165], v[230:233], v[102:105]
	v_mfma_f32_16x16x32_f16 v[98:101], v[170:173], v[230:233], v[98:101]
	s_setprio 0
	s_barrier
	v_lshl_add_u64 v[228:229], v[252:253], 0, s[30:31]
	s_mov_b32 m0, s80
	ds_read_b128 v[234:237], v146
	ds_read_b128 v[238:241], v146 offset:1024
	ds_read_b128 v[242:245], v146 offset:2048
	ds_read_b128 v[246:249], v146 offset:3072
	global_load_lds_dwordx4 v[228:229], off
	s_mov_b32 m0, s81
	v_lshl_add_u64 v[228:229], v[254:255], 0, s[30:31]
	global_load_lds_dwordx4 v[228:229], off
	s_barrier
	s_waitcnt lgkmcnt(0)
	s_setprio 1
	s_waitcnt lgkmcnt(0)
	v_mfma_f32_16x16x32_f16 v[94:97], v[234:237], v[174:177], v[94:97]
	v_mfma_f32_16x16x32_f16 v[90:93], v[242:245], v[174:177], v[90:93]
	v_mfma_f32_16x16x32_f16 v[86:89], v[234:237], v[182:185], v[86:89]
	v_mfma_f32_16x16x32_f16 v[82:85], v[242:245], v[182:185], v[82:85]
	v_mfma_f32_16x16x32_f16 v[74:77], v[234:237], v[190:193], v[74:77]
	v_mfma_f32_16x16x32_f16 v[66:69], v[242:245], v[190:193], v[66:69]
	v_mfma_f32_16x16x32_f16 v[62:65], v[234:237], v[198:201], v[62:65]
	v_mfma_f32_16x16x32_f16 v[58:61], v[242:245], v[198:201], v[58:61]
	v_mfma_f32_16x16x32_f16 v[94:97], v[238:241], v[178:181], v[94:97]
	v_mfma_f32_16x16x32_f16 v[90:93], v[246:249], v[178:181], v[90:93]
	v_mfma_f32_16x16x32_f16 v[86:89], v[238:241], v[186:189], v[86:89]
	v_mfma_f32_16x16x32_f16 v[82:85], v[246:249], v[186:189], v[82:85]
	v_mfma_f32_16x16x32_f16 v[74:77], v[238:241], v[194:197], v[74:77]
	v_mfma_f32_16x16x32_f16 v[66:69], v[246:249], v[194:197], v[66:69]
	v_mfma_f32_16x16x32_f16 v[62:65], v[238:241], v[230:233], v[62:65]
	v_mfma_f32_16x16x32_f16 v[58:61], v[246:249], v[230:233], v[58:61]
	s_setprio 0
	v_lshl_add_u64 v[212:213], v[212:213], 0, s[30:31]
	s_mov_b32 m0, s82
	s_barrier
	ds_read_b128 v[174:177], v145 offset:49152
	ds_read_b128 v[178:181], v145 offset:50176
	ds_read_b128 v[182:185], v144 offset:49152
	ds_read_b128 v[186:189], v144 offset:50176
	ds_read_b128 v[190:193], v143 offset:49152
	ds_read_b128 v[194:197], v143 offset:50176
	ds_read_b128 v[198:201], v142 offset:49152
	ds_read_b128 v[230:233], v142 offset:50176
	global_load_lds_dwordx4 v[212:213], off
	s_mov_b32 m0, s83
	v_lshl_add_u64 v[212:213], v[250:251], 0, s[30:31]
	global_load_lds_dwordx4 v[212:213], off
	s_barrier
	s_waitcnt lgkmcnt(0)
	s_setprio 1
	s_waitcnt lgkmcnt(0)
	v_mfma_f32_16x16x32_f16 v[54:57], v[158:161], v[174:177], v[54:57]
	v_mfma_f32_16x16x32_f16 v[50:53], v[166:169], v[174:177], v[50:53]
	v_mfma_f32_16x16x32_f16 v[46:49], v[158:161], v[182:185], v[46:49]
	v_mfma_f32_16x16x32_f16 v[42:45], v[166:169], v[182:185], v[42:45]
	v_mfma_f32_16x16x32_f16 v[38:41], v[158:161], v[190:193], v[38:41]
	v_mfma_f32_16x16x32_f16 v[34:37], v[166:169], v[190:193], v[34:37]
	v_mfma_f32_16x16x32_f16 v[30:33], v[158:161], v[198:201], v[30:33]
	v_mfma_f32_16x16x32_f16 v[26:29], v[166:169], v[198:201], v[26:29]
	v_mfma_f32_16x16x32_f16 v[54:57], v[162:165], v[178:181], v[54:57]
	v_mfma_f32_16x16x32_f16 v[50:53], v[170:173], v[178:181], v[50:53]
	v_mfma_f32_16x16x32_f16 v[46:49], v[162:165], v[186:189], v[46:49]
	v_mfma_f32_16x16x32_f16 v[42:45], v[170:173], v[186:189], v[42:45]
	v_mfma_f32_16x16x32_f16 v[38:41], v[162:165], v[194:197], v[38:41]
	v_mfma_f32_16x16x32_f16 v[34:37], v[170:173], v[194:197], v[34:37]
	v_mfma_f32_16x16x32_f16 v[30:33], v[162:165], v[230:233], v[30:33]
	v_mfma_f32_16x16x32_f16 v[26:29], v[170:173], v[230:233], v[26:29]
	s_setprio 0
	s_barrier
	s_mov_b32 m0, s84
	v_lshl_add_u64 v[158:159], v[252:253], 0, s[34:35]
	global_load_lds_dwordx4 v[158:159], off
	s_mov_b32 m0, s85
	v_lshl_add_u64 v[158:159], v[254:255], 0, s[34:35]
	global_load_lds_dwordx4 v[158:159], off
	s_waitcnt vmcnt(6)
	s_barrier
	s_setprio 1
	v_mfma_f32_16x16x32_f16 v[22:25], v[234:237], v[174:177], v[22:25]
	v_mfma_f32_16x16x32_f16 v[18:21], v[242:245], v[174:177], v[18:21]
	v_mfma_f32_16x16x32_f16 v[14:17], v[234:237], v[182:185], v[14:17]
	v_mfma_f32_16x16x32_f16 v[10:13], v[242:245], v[182:185], v[10:13]
	v_mfma_f32_16x16x32_f16 v[6:9], v[234:237], v[190:193], v[6:9]
	v_mfma_f32_16x16x32_f16 v[2:5], v[242:245], v[190:193], v[2:5]
	v_mfma_f32_16x16x32_f16 v[70:73], v[234:237], v[198:201], v[70:73]
	v_mfma_f32_16x16x32_f16 v[78:81], v[242:245], v[198:201], v[78:81]
	v_mfma_f32_16x16x32_f16 v[22:25], v[238:241], v[178:181], v[22:25]
	v_mfma_f32_16x16x32_f16 v[18:21], v[246:249], v[178:181], v[18:21]
	v_mfma_f32_16x16x32_f16 v[14:17], v[238:241], v[186:189], v[14:17]
	v_mfma_f32_16x16x32_f16 v[10:13], v[246:249], v[186:189], v[10:13]
	v_mfma_f32_16x16x32_f16 v[6:9], v[238:241], v[194:197], v[6:9]
	v_mfma_f32_16x16x32_f16 v[2:5], v[246:249], v[194:197], v[2:5]
	v_mfma_f32_16x16x32_f16 v[70:73], v[238:241], v[230:233], v[70:73]
	v_mfma_f32_16x16x32_f16 v[78:81], v[246:249], v[230:233], v[78:81]
	s_setprio 0
	s_add_i32 s3, s3, 2
	v_lshl_add_u64 v[134:135], v[134:135], 0, s[26:27]
	v_lshl_add_u64 v[136:137], v[136:137], 0, s[26:27]
	v_lshl_add_u64 v[138:139], v[138:139], 0, s[26:27]
	s_cmp_lt_u32 s3, 28
	v_lshl_add_u64 v[140:141], v[140:141], 0, s[26:27]
	s_barrier
	s_cbranch_scc1 .LBB1_67
	v_add_u32_e32 v147, 0xc000, v218
	s_mov_b64 s[0:1], 0xf80
	v_readfirstlane_b32 s3, v147
	v_lshl_add_u64 v[130:131], v[130:131], 0, s[0:1]
	s_mov_b32 m0, s3
	ds_read_b128 v[134:137], v156
	ds_read_b128 v[138:141], v156 offset:1024
	ds_read_b128 v[150:153], v156 offset:2048
	ds_read_b128 v[156:159], v156 offset:3072
	global_load_lds_dwordx4 v[130:131], off
	v_lshl_add_u64 v[130:131], v[132:133], 0, s[0:1]
	v_add_u32_e32 v132, 0xe000, v218
	s_nop 0
	v_readfirstlane_b32 s0, v132
	s_mov_b32 m0, s0
	s_nop 0
	global_load_lds_dwordx4 v[130:131], off
	ds_read_b128 v[130:133], v145
	ds_read_b128 v[160:163], v145 offset:1024
	ds_read_b128 v[164:167], v144
	ds_read_b128 v[168:171], v144 offset:1024
	ds_read_b128 v[172:175], v143
	ds_read_b128 v[176:179], v143 offset:1024
	ds_read_b128 v[180:183], v142
	ds_read_b128 v[184:187], v142 offset:1024
	s_barrier
	s_waitcnt lgkmcnt(0)
	s_setprio 1
	s_waitcnt lgkmcnt(0)
	v_mfma_f32_16x16x32_f16 v[126:129], v[134:137], v[130:133], v[126:129]
	v_mfma_f32_16x16x32_f16 v[118:121], v[134:137], v[164:167], v[118:121]
	v_mfma_f32_16x16x32_f16 v[110:113], v[134:137], v[172:175], v[110:113]
	v_mfma_f32_16x16x32_f16 v[106:109], v[150:153], v[172:175], v[106:109]
	v_mfma_f32_16x16x32_f16 v[126:129], v[138:141], v[160:163], v[126:129]
	v_mfma_f32_16x16x32_f16 v[122:125], v[150:153], v[130:133], v[122:125]
	v_mfma_f32_16x16x32_f16 v[118:121], v[138:141], v[168:171], v[118:121]
	v_mfma_f32_16x16x32_f16 v[114:117], v[150:153], v[164:167], v[114:117]
	v_mfma_f32_16x16x32_f16 v[110:113], v[138:141], v[176:179], v[110:113]
	v_mfma_f32_16x16x32_f16 v[106:109], v[156:159], v[176:179], v[106:109]
	v_mfma_f32_16x16x32_f16 v[102:105], v[134:137], v[180:183], v[102:105]
	v_mfma_f32_16x16x32_f16 v[98:101], v[150:153], v[180:183], v[98:101]
	v_mfma_f32_16x16x32_f16 v[188:191], v[156:159], v[160:163], v[122:125]
	v_mfma_f32_16x16x32_f16 v[192:195], v[156:159], v[168:171], v[114:117]
	v_mfma_f32_16x16x32_f16 v[196:199], v[138:141], v[184:187], v[102:105]
	v_mfma_f32_16x16x32_f16 v[230:233], v[156:159], v[184:187], v[98:101]
	s_setprio 0
	s_barrier
	s_nop 1
	ds_read_b128 v[98:101], v155
	ds_read_b128 v[102:105], v155 offset:1024
	ds_read_b128 v[114:117], v155 offset:2048
	ds_read_b128 v[122:125], v155 offset:3072
	s_barrier
	s_waitcnt lgkmcnt(0)
	s_setprio 1
	s_waitcnt lgkmcnt(0)
	v_mfma_f32_16x16x32_f16 v[94:97], v[98:101], v[130:133], v[94:97]
	v_mfma_f32_16x16x32_f16 v[90:93], v[114:117], v[130:133], v[90:93]
	v_mfma_f32_16x16x32_f16 v[74:77], v[98:101], v[172:175], v[74:77]
	v_mfma_f32_16x16x32_f16 v[66:69], v[114:117], v[172:175], v[66:69]
	v_mfma_f32_16x16x32_f16 v[62:65], v[98:101], v[180:183], v[62:65]
	v_mfma_f32_16x16x32_f16 v[94:97], v[102:105], v[160:163], v[94:97]
	v_mfma_f32_16x16x32_f16 v[90:93], v[122:125], v[160:163], v[90:93]
	v_mfma_f32_16x16x32_f16 v[86:89], v[98:101], v[164:167], v[86:89]
	v_mfma_f32_16x16x32_f16 v[82:85], v[114:117], v[164:167], v[82:85]
	v_mfma_f32_16x16x32_f16 v[74:77], v[102:105], v[176:179], v[74:77]
	v_mfma_f32_16x16x32_f16 v[66:69], v[122:125], v[176:179], v[66:69]
	v_mfma_f32_16x16x32_f16 v[62:65], v[102:105], v[184:187], v[62:65]
	v_mfma_f32_16x16x32_f16 v[58:61], v[114:117], v[180:183], v[58:61]
	v_mfma_f32_16x16x32_f16 v[130:133], v[102:105], v[168:171], v[86:89]
	v_mfma_f32_16x16x32_f16 v[160:163], v[122:125], v[168:171], v[82:85]
	v_mfma_f32_16x16x32_f16 v[164:167], v[122:125], v[184:187], v[58:61]
	s_setprio 0
	s_barrier
	s_nop 2
	ds_read_b128 v[58:61], v145 offset:16384
	ds_read_b128 v[82:85], v145 offset:17408
	ds_read_b128 v[86:89], v144 offset:16384
	ds_read_b128 v[168:171], v144 offset:17408
	ds_read_b128 v[172:175], v143 offset:16384
	ds_read_b128 v[176:179], v143 offset:17408
	ds_read_b128 v[180:183], v142 offset:16384
	ds_read_b128 v[184:187], v142 offset:17408
	s_waitcnt vmcnt(4)
	s_barrier
	s_waitcnt lgkmcnt(0)
	s_setprio 1
	s_waitcnt lgkmcnt(0)
	v_mfma_f32_16x16x32_f16 v[54:57], v[134:137], v[58:61], v[54:57]
	v_mfma_f32_16x16x32_f16 v[50:53], v[150:153], v[58:61], v[50:53]
	v_mfma_f32_16x16x32_f16 v[46:49], v[134:137], v[86:89], v[46:49]
	v_mfma_f32_16x16x32_f16 v[42:45], v[150:153], v[86:89], v[42:45]
	v_mfma_f32_16x16x32_f16 v[38:41], v[134:137], v[172:175], v[38:41]
	v_mfma_f32_16x16x32_f16 v[26:29], v[150:153], v[180:183], v[26:29]
	v_mfma_f32_16x16x32_f16 v[54:57], v[138:141], v[82:85], v[54:57]
	v_mfma_f32_16x16x32_f16 v[50:53], v[156:159], v[82:85], v[50:53]
	v_mfma_f32_16x16x32_f16 v[46:49], v[138:141], v[168:171], v[46:49]
	v_mfma_f32_16x16x32_f16 v[42:45], v[156:159], v[168:171], v[42:45]
	v_mfma_f32_16x16x32_f16 v[38:41], v[138:141], v[176:179], v[38:41]
	v_mfma_f32_16x16x32_f16 v[34:37], v[150:153], v[172:175], v[34:37]
	v_mfma_f32_16x16x32_f16 v[30:33], v[134:137], v[180:183], v[30:33]
	v_mfma_f32_16x16x32_f16 v[26:29], v[156:159], v[184:187], v[26:29]
	v_mfma_f32_16x16x32_f16 v[234:237], v[156:159], v[176:179], v[34:37]
	v_mfma_f32_16x16x32_f16 v[134:137], v[138:141], v[184:187], v[30:33]
	s_setprio 0
	s_setprio 1
	v_mfma_f32_16x16x32_f16 v[2:5], v[114:117], v[172:175], v[2:5]
	v_mfma_f32_16x16x32_f16 v[22:25], v[98:101], v[58:61], v[22:25]
	v_mfma_f32_16x16x32_f16 v[14:17], v[98:101], v[86:89], v[14:17]
	v_mfma_f32_16x16x32_f16 v[10:13], v[114:117], v[86:89], v[10:13]
	v_mfma_f32_16x16x32_f16 v[6:9], v[98:101], v[172:175], v[6:9]
	v_mfma_f32_16x16x32_f16 v[154:157], v[122:125], v[176:179], v[2:5]
	v_mfma_f32_16x16x32_f16 v[2:5], v[98:101], v[180:183], v[70:73]
	v_mfma_f32_16x16x32_f16 v[22:25], v[102:105], v[82:85], v[22:25]
	v_mfma_f32_16x16x32_f16 v[18:21], v[114:117], v[58:61], v[18:21]
	v_mfma_f32_16x16x32_f16 v[150:153], v[102:105], v[168:171], v[14:17]
	v_mfma_f32_16x16x32_f16 v[10:13], v[122:125], v[168:171], v[10:13]
	v_mfma_f32_16x16x32_f16 v[6:9], v[102:105], v[176:179], v[6:9]
	v_mfma_f32_16x16x32_f16 v[168:171], v[102:105], v[184:187], v[2:5]
	v_mfma_f32_16x16x32_f16 v[2:5], v[114:117], v[180:183], v[78:81]
	v_mfma_f32_16x16x32_f16 v[138:141], v[122:125], v[82:85], v[18:21]
	v_mfma_f32_16x16x32_f16 v[172:175], v[122:125], v[184:187], v[2:5]
	s_setprio 0
	s_barrier
	s_nop 3
	ds_read_b128 v[2:5], v148
	ds_read_b128 v[14:17], v148 offset:1024
	ds_read_b128 v[176:179], v148 offset:2048
	ds_read_b128 v[180:183], v148 offset:3072
	ds_read_b128 v[18:21], v145 offset:32768
	ds_read_b128 v[30:33], v145 offset:33792
	ds_read_b128 v[34:37], v144 offset:32768
	ds_read_b128 v[78:81], v144 offset:33792
	ds_read_b128 v[184:187], v143 offset:32768
	ds_read_b128 v[238:241], v143 offset:33792
	ds_read_b128 v[242:245], v142 offset:32768
	ds_read_b128 v[246:249], v142 offset:33792
	s_waitcnt vmcnt(2)
	s_barrier
	s_waitcnt lgkmcnt(0)
	s_setprio 1
	s_waitcnt lgkmcnt(0)
	v_mfma_f32_16x16x32_f16 v[58:61], v[2:5], v[18:21], v[126:129]
	v_mfma_f32_16x16x32_f16 v[122:125], v[14:17], v[30:33], v[58:61]
	v_mfma_f32_16x16x32_f16 v[58:61], v[176:179], v[18:21], v[188:191]
	v_mfma_f32_16x16x32_f16 v[114:117], v[180:183], v[30:33], v[58:61]
	v_mfma_f32_16x16x32_f16 v[58:61], v[2:5], v[34:37], v[118:121]
	v_mfma_f32_16x16x32_f16 v[102:105], v[14:17], v[78:81], v[58:61]
	v_mfma_f32_16x16x32_f16 v[58:61], v[176:179], v[34:37], v[192:195]
	v_mfma_f32_16x16x32_f16 v[98:101], v[180:183], v[78:81], v[58:61]
	v_mfma_f32_16x16x32_f16 v[58:61], v[2:5], v[184:187], v[110:113]
	v_mfma_f32_16x16x32_f16 v[86:89], v[14:17], v[238:241], v[58:61]
	v_mfma_f32_16x16x32_f16 v[58:61], v[176:179], v[184:187], v[106:109]
	v_mfma_f32_16x16x32_f16 v[82:85], v[180:183], v[238:241], v[58:61]
	v_mfma_f32_16x16x32_f16 v[58:61], v[2:5], v[242:245], v[196:199]
	v_mfma_f32_16x16x32_f16 v[70:73], v[14:17], v[246:249], v[58:61]
	v_mfma_f32_16x16x32_f16 v[58:61], v[176:179], v[242:245], v[230:233]
	v_mfma_f32_16x16x32_f16 v[58:61], v[180:183], v[246:249], v[58:61]
	s_setprio 0
	s_barrier
	ds_read_b128 v[188:191], v146
	ds_read_b128 v[192:195], v146 offset:1024
	ds_read_b128 v[196:199], v146 offset:2048
	ds_read_b128 v[146:149], v146 offset:3072
	s_waitcnt vmcnt(0)
	s_barrier
	s_waitcnt lgkmcnt(0)
	s_setprio 1
	s_waitcnt lgkmcnt(0)
	v_mfma_f32_16x16x32_f16 v[94:97], v[188:191], v[18:21], v[94:97]
	v_mfma_f32_16x16x32_f16 v[18:21], v[196:199], v[18:21], v[90:93]
	v_mfma_f32_16x16x32_f16 v[118:121], v[146:149], v[30:33], v[18:21]
	v_mfma_f32_16x16x32_f16 v[18:21], v[188:191], v[34:37], v[130:133]
	v_mfma_f32_16x16x32_f16 v[110:113], v[192:195], v[78:81], v[18:21]
	v_mfma_f32_16x16x32_f16 v[18:21], v[196:199], v[34:37], v[160:163]
	v_mfma_f32_16x16x32_f16 v[106:109], v[146:149], v[78:81], v[18:21]
	v_mfma_f32_16x16x32_f16 v[18:21], v[188:191], v[184:187], v[74:77]
	v_mfma_f32_16x16x32_f16 v[126:129], v[192:195], v[30:33], v[94:97]
	v_mfma_f32_16x16x32_f16 v[94:97], v[192:195], v[238:241], v[18:21]
	v_mfma_f32_16x16x32_f16 v[18:21], v[196:199], v[184:187], v[66:69]
	v_mfma_f32_16x16x32_f16 v[90:93], v[146:149], v[238:241], v[18:21]
	v_mfma_f32_16x16x32_f16 v[18:21], v[188:191], v[242:245], v[62:65]
	v_mfma_f32_16x16x32_f16 v[78:81], v[192:195], v[246:249], v[18:21]
	v_mfma_f32_16x16x32_f16 v[18:21], v[196:199], v[242:245], v[164:167]
	v_mfma_f32_16x16x32_f16 v[74:77], v[146:149], v[246:249], v[18:21]
	s_setprio 0
	s_barrier
	ds_read_b128 v[130:133], v145 offset:49152
	ds_read_b128 v[158:161], v145 offset:50176
	ds_read_b128 v[162:165], v144 offset:49152
	ds_read_b128 v[184:187], v144 offset:50176
	ds_read_b128 v[230:233], v143 offset:49152
	ds_read_b128 v[238:241], v143 offset:50176
	ds_read_b128 v[242:245], v142 offset:49152
	ds_read_b128 v[142:145], v142 offset:50176
	s_barrier
	s_waitcnt lgkmcnt(0)
	s_setprio 1
	s_waitcnt lgkmcnt(0)
	v_mfma_f32_16x16x32_f16 v[18:21], v[2:5], v[130:133], v[54:57]
	v_mfma_f32_16x16x32_f16 v[66:69], v[14:17], v[158:161], v[18:21]
	v_mfma_f32_16x16x32_f16 v[18:21], v[176:179], v[130:133], v[50:53]
	v_mfma_f32_16x16x32_f16 v[50:53], v[180:183], v[158:161], v[18:21]
	v_mfma_f32_16x16x32_f16 v[18:21], v[2:5], v[162:165], v[46:49]
	v_mfma_f32_16x16x32_f16 v[46:49], v[14:17], v[184:187], v[18:21]
	v_mfma_f32_16x16x32_f16 v[18:21], v[176:179], v[162:165], v[42:45]
	v_mfma_f32_16x16x32_f16 v[34:37], v[180:183], v[184:187], v[18:21]
	v_mfma_f32_16x16x32_f16 v[18:21], v[2:5], v[230:233], v[38:41]
	v_mfma_f32_16x16x32_f16 v[2:5], v[2:5], v[242:245], v[134:137]
	v_mfma_f32_16x16x32_f16 v[30:33], v[14:17], v[238:241], v[18:21]
	v_mfma_f32_16x16x32_f16 v[18:21], v[176:179], v[230:233], v[234:237]
	v_mfma_f32_16x16x32_f16 v[14:17], v[14:17], v[142:145], v[2:5]
	v_mfma_f32_16x16x32_f16 v[2:5], v[176:179], v[242:245], v[26:29]
	v_mfma_f32_16x16x32_f16 v[18:21], v[180:183], v[238:241], v[18:21]
	v_mfma_f32_16x16x32_f16 v[2:5], v[180:183], v[142:145], v[2:5]
	s_setprio 0
	s_setprio 1
	v_mfma_f32_16x16x32_f16 v[22:25], v[188:191], v[130:133], v[22:25]
	v_mfma_f32_16x16x32_f16 v[62:65], v[192:195], v[158:161], v[22:25]
	v_mfma_f32_16x16x32_f16 v[22:25], v[196:199], v[130:133], v[138:141]
	v_mfma_f32_16x16x32_f16 v[6:9], v[188:191], v[230:233], v[6:9]
	v_mfma_f32_16x16x32_f16 v[54:57], v[146:149], v[158:161], v[22:25]
	v_mfma_f32_16x16x32_f16 v[22:25], v[188:191], v[162:165], v[150:153]
	v_mfma_f32_16x16x32_f16 v[26:29], v[192:195], v[238:241], v[6:9]
	v_mfma_f32_16x16x32_f16 v[6:9], v[196:199], v[230:233], v[154:157]
	v_mfma_f32_16x16x32_f16 v[42:45], v[192:195], v[184:187], v[22:25]
	v_mfma_f32_16x16x32_f16 v[10:13], v[196:199], v[162:165], v[10:13]
	v_mfma_f32_16x16x32_f16 v[22:25], v[146:149], v[238:241], v[6:9]
	v_mfma_f32_16x16x32_f16 v[6:9], v[188:191], v[242:245], v[168:171]
	v_mfma_f32_16x16x32_f16 v[38:41], v[146:149], v[184:187], v[10:13]
	v_mfma_f32_16x16x32_f16 v[10:13], v[192:195], v[142:145], v[6:9]
	v_mfma_f32_16x16x32_f16 v[6:9], v[196:199], v[242:245], v[172:175]
	v_mfma_f32_16x16x32_f16 v[6:9], v[146:149], v[142:145], v[6:9]
	s_setprio 0
	s_movk_i32 s0, 0x100
	v_cmp_gt_u32_e64 s[0:1], s0, v0
	s_barrier
	s_and_saveexec_b64 s[26:27], s[0:1]
	s_cbranch_execz .LBB1_70
	s_barrier

.LBB3_8:
	s_waitcnt lgkmcnt(0)
	s_nop 1
	s_nop 0
	v_mfma_f32_32x32x16_f16 v[80:95], a[192:195], a[128:131], 0
	s_nop 0
	v_mfma_f32_32x32x16_f16 v[48:63], a[192:195], a[160:163], 0
	s_nop 0
	v_mfma_f32_32x32x16_f16 v[64:79], a[224:227], a[128:131], 0
	s_nop 0
	v_mfma_f32_32x32x16_f16 v[32:47], a[224:227], a[160:163], 0
	s_nop 0
	v_mfma_f32_32x32x16_f16 v[80:95], a[196:199], a[132:135], v[80:95]
	s_nop 0
	v_mfma_f32_32x32x16_f16 v[48:63], a[196:199], a[164:167], v[48:63]
	s_nop 0
	v_mfma_f32_32x32x16_f16 v[64:79], a[228:231], a[132:135], v[64:79]
	s_nop 0
	v_mfma_f32_32x32x16_f16 v[32:47], a[228:231], a[164:167], v[32:47]
	s_nop 0
	v_mfma_f32_32x32x16_f16 v[80:95], a[200:203], a[136:139], v[80:95]
	s_nop 0
	v_mfma_f32_32x32x16_f16 v[48:63], a[200:203], a[168:171], v[48:63]
	s_nop 0
	v_mfma_f32_32x32x16_f16 v[64:79], a[232:235], a[136:139], v[64:79]
	s_nop 0
	v_mfma_f32_32x32x16_f16 v[32:47], a[232:235], a[168:171], v[32:47]
	s_nop 0
	v_mfma_f32_32x32x16_f16 v[80:95], a[204:207], a[140:143], v[80:95]
	s_nop 0
	v_mfma_f32_32x32x16_f16 v[48:63], a[204:207], a[172:175], v[48:63]
	s_nop 0
	v_mfma_f32_32x32x16_f16 v[64:79], a[236:239], a[140:143], v[64:79]
	s_nop 0
	v_mfma_f32_32x32x16_f16 v[32:47], a[236:239], a[172:175], v[32:47]
	s_nop 0
	v_mfma_f32_32x32x16_f16 v[80:95], a[208:211], a[144:147], v[80:95]
	s_mov_b32 s0, s33
	v_mfma_f32_32x32x16_f16 v[48:63], a[208:211], a[176:179], v[48:63]
	s_mov_b32 s1, s40
	v_mfma_f32_32x32x16_f16 v[64:79], a[240:243], a[144:147], v[64:79]
	s_mov_b32 s12, s41
	v_mfma_f32_32x32x16_f16 v[32:47], a[240:243], a[176:179], v[32:47]
	s_mov_b32 s13, s42
	v_mfma_f32_32x32x16_f16 v[80:95], a[212:215], a[148:151], v[80:95]
	s_mov_b32 s22, s43
	v_mfma_f32_32x32x16_f16 v[48:63], a[212:215], a[180:183], v[48:63]
	s_mov_b32 s23, s44
	v_mfma_f32_32x32x16_f16 v[64:79], a[244:247], a[148:151], v[64:79]
	s_mov_b32 s24, s45
	v_mfma_f32_32x32x16_f16 v[32:47], a[244:247], a[180:183], v[32:47]
	s_mov_b32 s30, s46
	v_mfma_f32_32x32x16_f16 v[80:95], a[216:219], a[152:155], v[80:95]
	s_mov_b32 s31, s47
	v_mfma_f32_32x32x16_f16 v[48:63], a[216:219], a[184:187], v[48:63]
	s_mov_b32 s34, s48
	v_mfma_f32_32x32x16_f16 v[64:79], a[248:251], a[152:155], v[64:79]
	s_mov_b32 s35, s49
	v_mfma_f32_32x32x16_f16 v[32:47], a[248:251], a[184:187], v[32:47]
	s_mov_b32 s91, s50
	v_mfma_f32_32x32x16_f16 v[80:95], a[220:223], a[156:159], v[80:95]
	s_mov_b32 s92, s51
	v_mfma_f32_32x32x16_f16 v[48:63], a[220:223], a[188:191], v[48:63]
	s_mov_b32 s93, s52
	v_mfma_f32_32x32x16_f16 v[64:79], a[252:255], a[156:159], v[64:79]
	s_mov_b32 s94, s53
	v_mfma_f32_32x32x16_f16 v[32:47], a[252:255], a[188:191], v[32:47]
	s_mov_b32 s95, s54
	s_nop 0
	s_nop 4
	s_waitcnt vmcnt(0) lgkmcnt(0)
	s_barrier
	s_nop 0
	s_mov_b32 m0, s0
	s_nop 0
	buffer_load_dwordx4 v211, s[16:19], s1 offen lds
	s_nop 0
	s_mov_b32 m0, s12
	s_nop 0
	buffer_load_dwordx4 v212, s[16:19], s13 offen lds
	ds_read_b128 a[192:195], v221 offset:0
	s_nop 0
	s_mov_b32 m0, s22
	s_nop 0
	buffer_load_dwordx4 v211, s[16:19], s23 offen lds
	ds_read_b128 a[196:199], v222 offset:0
	s_nop 0
	s_mov_b32 m0, s24
	s_nop 0
	buffer_load_dwordx4 v212, s[16:19], s30 offen lds
	ds_read_b128 a[200:203], v223 offset:0
	s_mov_b32 s22, s18
	s_mov_b32 s23, s19
	s_mov_b32 m0, s31
	s_nop 0
	buffer_load_dwordx4 v213, s[20:23], s34 offen lds
	ds_read_b128 a[204:207], v224 offset:0
	s_nop 0
	s_mov_b32 m0, s35
	s_nop 0
	buffer_load_dwordx4 v213, s[20:23], s91 offen lds
	ds_read_b128 a[208:211], v221 offset:128
	s_nop 0
	s_mov_b32 m0, s92
	s_nop 0
	buffer_load_dwordx4 v213, s[20:23], s93 offen lds
	ds_read_b128 a[212:215], v222 offset:128
	s_nop 0
	s_mov_b32 m0, s94
	s_nop 0
	buffer_load_dwordx4 v213, s[20:23], s95 offen lds
	ds_read_b128 a[216:219], v223 offset:128
	s_nop 0
	ds_read_b128 a[220:223], v224 offset:128
	v_max3_f32 v96, v80, v81, v64
	v_max3_f32 v97, v82, v83, v65
	s_nop 0
	v_max3_f32 v96, v96, v66, v67
	ds_read_b128 a[224:227], v221 offset:8192
	s_nop 0
	v_max3_f32 v96, v96, v84, v85
	v_max3_f32 v97, v97, v86, v87
	s_nop 0
	v_max3_f32 v96, v96, v68, v69
	v_max3_f32 v97, v97, v70, v71
	ds_read_b128 a[228:231], v222 offset:8192
	s_nop 0
	v_max3_f32 v96, v96, v88, v89
	v_max3_f32 v97, v97, v90, v91
	s_nop 0
	v_max3_f32 v96, v96, v72, v73
	v_max3_f32 v97, v97, v74, v75
	ds_read_b128 a[232:235], v223 offset:8192
	s_nop 0
	v_max3_f32 v96, v96, v92, v93
	v_max3_f32 v97, v97, v94, v95
	s_nop 0
	v_max3_f32 v96, v96, v76, v77
	v_max3_f32 v97, v97, v78, v79
	ds_read_b128 a[236:239], v224 offset:8192
	v_max3_f32 v98, v48, v49, v32
	v_max3_f32 v99, v50, v51, v33
	s_nop 0
	v_max3_f32 v98, v98, v34, v35
	ds_read_b128 a[240:243], v221 offset:8320
	s_nop 0
	v_max3_f32 v98, v98, v52, v53
	v_max3_f32 v99, v99, v54, v55
	s_nop 0
	v_max3_f32 v98, v98, v36, v37
	v_max3_f32 v99, v99, v38, v39
	ds_read_b128 a[244:247], v222 offset:8320
	s_nop 0
	v_max3_f32 v98, v98, v56, v57
	v_max3_f32 v99, v99, v58, v59
	s_nop 0
	v_max3_f32 v98, v98, v40, v41
	v_max3_f32 v99, v99, v42, v43
	ds_read_b128 a[248:251], v223 offset:8320
	s_nop 0
	v_max3_f32 v98, v98, v60, v61
	v_max3_f32 v99, v99, v62, v63
	s_nop 0
	v_max3_f32 v98, v98, v44, v45
	v_max3_f32 v99, v99, v46, v47
	ds_read_b128 a[252:255], v224 offset:8320
	v_max_f32_e32 v96, v96, v97
	s_nop 0
	v_mov_b32_e32 v97, v96
	s_nop 1
	v_permlane32_swap_b32_e32 v96, v97
	v_max_f32_e32 v229, v96, v97
	v_max_f32_e32 v96, v98, v99
	s_nop 0
	v_mov_b32_e32 v97, v96
	s_nop 1
	v_permlane32_swap_b32_e32 v96, v97
	v_max_f32_e32 v200, v96, v97
	v_sub_f32_e32 v128, v66, v229
	v_mbcnt_lo_u32_b32 v66, -1, 0
	v_mbcnt_hi_u32_b32 v66, -1, v66
	v_sub_f32_e32 v129, v67, v229
	v_xor_b32_e32 v67, 0x80000000, v229
	v_cmp_gt_u32_e32 vcc, 32, v66
	v_sub_f32_e32 v142, v32, v200
	v_mov_b32_e32 v230, 1.0
	v_sub_f32_e32 v143, v33, v200
	v_xor_b32_e32 v33, 0x80000000, v200
	v_cndmask_b32_e64 v66, 0, 1.0, vcc
	s_nop 1
	v_mfma_f32_32x32x2_f32 v[16:31], v66, v67, 0
	v_mbcnt_lo_u32_b32 v32, -1, 0
	v_mbcnt_hi_u32_b32 v32, -1, v32
	v_sub_f32_e32 v80, v80, v229
	v_sub_f32_e32 v81, v81, v229
	v_sub_f32_e32 v82, v82, v229
	v_sub_f32_e32 v83, v83, v229
	v_sub_f32_e32 v84, v84, v229
	v_sub_f32_e32 v85, v85, v229
	v_sub_f32_e32 v86, v86, v229
	v_sub_f32_e32 v87, v87, v229
	v_sub_f32_e32 v88, v88, v229
	v_sub_f32_e32 v89, v89, v229
	v_sub_f32_e32 v90, v90, v229
	v_sub_f32_e32 v91, v91, v229
	v_sub_f32_e32 v92, v92, v229
	v_sub_f32_e32 v93, v93, v229
	v_sub_f32_e32 v94, v94, v229
	v_sub_f32_e32 v95, v95, v229
	v_sub_f32_e32 v64, v64, v229
	v_sub_f32_e32 v65, v65, v229
	v_sub_f32_e32 v130, v68, v229
	s_nop 0
	v_cmp_gt_u32_e32 vcc, 32, v32
	v_sub_f32_e32 v131, v69, v229
	v_sub_f32_e32 v132, v70, v229
	v_sub_f32_e32 v133, v71, v229
	v_sub_f32_e32 v134, v72, v229
	v_sub_f32_e32 v135, v73, v229
	v_sub_f32_e32 v136, v74, v229
	v_sub_f32_e32 v137, v75, v229
	v_sub_f32_e32 v138, v76, v229
	v_sub_f32_e32 v139, v77, v229
	v_sub_f32_e32 v140, v78, v229
	v_sub_f32_e32 v141, v79, v229
	v_sub_f32_e32 v48, v48, v200
	v_sub_f32_e32 v49, v49, v200
	v_sub_f32_e32 v50, v50, v200
	v_sub_f32_e32 v51, v51, v200
	v_sub_f32_e32 v52, v52, v200
	v_sub_f32_e32 v53, v53, v200
	v_sub_f32_e32 v54, v54, v200
	v_sub_f32_e32 v55, v55, v200
	s_nop 1
	v_cndmask_b32_e64 v32, 0, 1.0, vcc
	v_sub_f32_e32 v56, v56, v200
	v_sub_f32_e32 v57, v57, v200
	v_sub_f32_e32 v58, v58, v200
	v_sub_f32_e32 v59, v59, v200
	v_sub_f32_e32 v60, v60, v200
	v_sub_f32_e32 v61, v61, v200
	v_sub_f32_e32 v62, v62, v200
	v_sub_f32_e32 v63, v63, v200
	v_sub_f32_e32 v144, v34, v200
	v_sub_f32_e32 v145, v35, v200
	v_sub_f32_e32 v146, v36, v200
	v_sub_f32_e32 v147, v37, v200
	v_sub_f32_e32 v183, v38, v200
	v_sub_f32_e32 v192, v39, v200
	v_sub_f32_e32 v193, v40, v200
	v_sub_f32_e32 v194, v41, v200
	v_sub_f32_e32 v195, v42, v200
	v_sub_f32_e32 v196, v43, v200
	v_sub_f32_e32 v197, v44, v200
	v_sub_f32_e32 v199, v45, v200
	v_sub_f32_e32 v231, v46, v200
	v_sub_f32_e32 v233, v47, v200
	s_nop 1
	v_mfma_f32_32x32x2_f32 v[0:15], v32, v33, 0
	v_exp_f32_e32 v112, v80
	v_exp_f32_e32 v113, v81
	v_exp_f32_e32 v114, v82
	v_exp_f32_e32 v115, v83
	v_add_f32_e32 v32, v201, v112
	v_add_f32_e32 v33, v201, v113
	v_exp_f32_e32 v116, v84
	v_exp_f32_e32 v117, v85
	v_exp_f32_e32 v118, v86
	v_add_f32_e32 v32, v32, v114
	v_add_f32_e32 v33, v33, v115
	v_exp_f32_e32 v119, v87
	v_exp_f32_e32 v120, v88
	v_add_f32_e32 v32, v32, v116
	v_add_f32_e32 v33, v33, v117
	s_nop 0
	v_add_f32_e32 v32, v32, v118
	v_exp_f32_e32 v121, v89
	v_exp_f32_e32 v122, v90
	v_exp_f32_e32 v123, v91
	v_add_f32_e32 v33, v33, v119
	v_add_f32_e32 v32, v32, v120
	v_exp_f32_e32 v124, v92
	v_exp_f32_e32 v125, v93
	v_add_f32_e32 v33, v33, v121
	v_add_f32_e32 v32, v32, v122
	s_nop 0
	v_add_f32_e32 v33, v33, v123
	v_exp_f32_e32 v126, v94
	v_exp_f32_e32 v127, v95
	v_exp_f32_e32 v96, v48
	v_add_f32_e32 v32, v32, v124
	v_add_f32_e32 v33, v33, v125
	v_exp_f32_e32 v97, v49
	v_exp_f32_e32 v98, v50
	v_add_f32_e32 v234, v32, v126
	v_add_f32_e32 v235, v33, v127
	v_add_f32_e32 v32, v201, v96
	v_exp_f32_e32 v99, v51
	v_exp_f32_e32 v100, v52
	v_exp_f32_e32 v101, v53
	v_add_f32_e32 v33, v201, v97
	v_add_f32_e32 v32, v32, v98
	v_exp_f32_e32 v102, v54
	v_exp_f32_e32 v103, v55
	v_add_f32_e32 v33, v33, v99
	v_add_f32_e32 v32, v32, v100
	s_nop 0
	v_add_f32_e32 v33, v33, v101
	v_exp_f32_e32 v104, v56
	v_exp_f32_e32 v105, v57
	v_exp_f32_e32 v106, v58
	v_add_f32_e32 v32, v32, v102
	v_add_f32_e32 v33, v33, v103
	v_exp_f32_e32 v107, v59
	v_exp_f32_e32 v108, v60
	v_add_f32_e32 v32, v32, v104
	v_add_f32_e32 v33, v33, v105
	s_nop 0
	v_add_f32_e32 v32, v32, v106
	v_exp_f32_e32 v109, v61
	v_exp_f32_e32 v110, v62
	v_exp_f32_e32 v111, v63
	v_add_f32_e32 v33, v33, v107
	v_add_f32_e32 v32, v32, v108
	s_nop 0
	s_waitcnt lgkmcnt(0)
	v_add_f32_e32 v33, v33, v109
	v_add_f32_e32 v236, v32, v110
	s_nop 0
	v_add_f32_e32 v237, v33, v111
	v_mfma_f32_32x32x16_f16 v[80:95], a[192:195], a[128:131], v[16:31]
	ds_read_b64_tr_b16 v[168:169], v210 offset:0
	v_exp_f32_e32 v238, v64
	v_exp_f32_e32 v239, v65
	v_cvt_pk_f16_f32 v152, v112, v113
	v_exp_f32_e32 v112, v128
	v_exp_f32_e32 v113, v129
	v_mfma_f32_32x32x16_f16 v[64:79], a[192:195], a[160:163], v[0:15]
	ds_read_b64_tr_b16 v[170:171], v210 offset:0x800
	v_cvt_pk_f16_f32 v153, v114, v115
	v_exp_f32_e32 v114, v130
	v_exp_f32_e32 v115, v131
	v_mfma_f32_32x32x16_f16 v[48:63], a[224:227], a[128:131], v[16:31]
	ds_read_b64_tr_b16 v[172:173], v210 offset:0x200
	v_cvt_pk_f16_f32 v154, v116, v117
	v_mfma_f32_32x32x16_f16 v[32:47], a[224:227], a[160:163], v[0:15]
	ds_read_b64_tr_b16 v[174:175], v210 offset:0xa00
	ds_read_b64_tr_b16 v[164:165], v210 offset:0x400
	v_exp_f32_e32 v240, v132
	v_exp_f32_e32 v241, v133
	v_cvt_pk_f16_f32 v155, v118, v119
	v_exp_f32_e32 v184, v134
	v_exp_f32_e32 v185, v135
	v_mfma_f32_32x32x16_f16 v[80:95], a[196:199], a[132:135], v[80:95]
	ds_read_b64_tr_b16 v[166:167], v210 offset:0xc00
	v_cvt_pk_f16_f32 v128, v120, v121
	v_exp_f32_e32 v186, v136
	v_exp_f32_e32 v187, v137
	v_mfma_f32_32x32x16_f16 v[64:79], a[196:199], a[164:167], v[64:79]
	ds_read_b64_tr_b16 v[176:177], v210 offset:0x600
	v_cvt_pk_f16_f32 v129, v122, v123
	v_exp_f32_e32 v188, v138
	v_exp_f32_e32 v189, v139
	v_mfma_f32_32x32x16_f16 v[48:63], a[228:231], a[132:135], v[48:63]
	ds_read_b64_tr_b16 v[178:179], v210 offset:0xe00
	v_cvt_pk_f16_f32 v130, v124, v125
	v_mfma_f32_32x32x16_f16 v[32:47], a[228:231], a[164:167], v[32:47]
	ds_read_b64_tr_b16 v[160:161], v210 offset:0x1000
	v_exp_f32_e32 v190, v140
	v_exp_f32_e32 v191, v141
	ds_read_b64_tr_b16 v[162:163], v210 offset:0x1800
	v_cvt_pk_f16_f32 v131, v126, v127
	v_exp_f32_e32 v141, v142
	v_exp_f32_e32 v142, v143
	v_mfma_f32_32x32x16_f16 v[80:95], a[200:203], a[136:139], v[80:95]
	ds_read_b64_tr_b16 v[156:157], v210 offset:0x1200
	v_cvt_pk_f16_f32 v180, v96, v97
	v_exp_f32_e32 v143, v144
	v_mfma_f32_32x32x16_f16 v[64:79], a[200:203], a[168:171], v[64:79]
	ds_read_b64_tr_b16 v[158:159], v210 offset:0x1a00
	v_exp_f32_e32 v242, v145
	v_cvt_pk_f16_f32 v181, v98, v99
	v_mfma_f32_32x32x16_f16 v[48:63], a[232:235], a[136:139], v[48:63]
	ds_read_b64_tr_b16 v[148:149], v210 offset:0x1400
	v_exp_f32_e32 v243, v146
	v_exp_f32_e32 v244, v147
	v_cvt_pk_f16_f32 v182, v100, v101
	v_mfma_f32_32x32x16_f16 v[32:47], a[232:235], a[168:171], v[32:47]
	ds_read_b64_tr_b16 v[150:151], v210 offset:0x1c00
	ds_read_b64_tr_b16 v[136:137], v210 offset:0x1600
	v_exp_f32_e32 v245, v183
	v_exp_f32_e32 v246, v192
	v_cvt_pk_f16_f32 v183, v102, v103
	v_exp_f32_e32 v192, v193
	v_exp_f32_e32 v193, v194
	v_mfma_f32_32x32x16_f16 v[80:95], a[204:207], a[140:143], v[80:95]
	ds_read_b64_tr_b16 v[138:139], v210 offset:0x1e00
	v_cvt_pk_f16_f32 v144, v104, v105
	v_exp_f32_e32 v194, v195
	v_exp_f32_e32 v195, v196
	v_mfma_f32_32x32x16_f16 v[64:79], a[204:207], a[172:175], v[64:79]
	ds_read_b64_tr_b16 v[132:133], v210 offset:0x2000
	v_cvt_pk_f16_f32 v145, v106, v107
	v_exp_f32_e32 v198, v197
	v_exp_f32_e32 v199, v199
	v_mfma_f32_32x32x16_f16 v[48:63], a[236:239], a[140:143], v[48:63]
	ds_read_b64_tr_b16 v[134:135], v210 offset:0x2800
	v_cvt_pk_f16_f32 v146, v108, v109
	v_mfma_f32_32x32x16_f16 v[32:47], a[236:239], a[172:175], v[32:47]
	ds_read_b64_tr_b16 v[124:125], v210 offset:0x2200
	v_exp_f32_e32 v232, v231
	v_exp_f32_e32 v233, v233
	ds_read_b64_tr_b16 v[126:127], v210 offset:0x2a00
	v_cvt_pk_f16_f32 v147, v110, v111
	s_mov_b32 s0, s55
	v_mfma_f32_32x32x16_f16 v[80:95], a[208:211], a[144:147], v[80:95]
	ds_read_b64_tr_b16 v[120:121], v210 offset:0x2400
	v_cvt_pk_f16_f32 v116, v238, v239
	v_add_f32_e32 v96, v234, v238
	v_add_f32_e32 v97, v235, v239
	s_mov_b32 s1, s56
	v_mfma_f32_32x32x16_f16 v[64:79], a[208:211], a[176:179], v[64:79]
	ds_read_b64_tr_b16 v[122:123], v210 offset:0x2c00
	v_cvt_pk_f16_f32 v117, v112, v113
	v_add_f32_e32 v96, v96, v112
	v_add_f32_e32 v97, v97, v113
	s_mov_b32 s12, s57
	v_mfma_f32_32x32x16_f16 v[48:63], a[240:243], a[144:147], v[48:63]
	ds_read_b64_tr_b16 v[112:113], v210 offset:0x2600
	v_cvt_pk_f16_f32 v118, v114, v115
	v_add_f32_e32 v96, v96, v114
	v_add_f32_e32 v97, v97, v115
	s_mov_b32 s13, s58
	v_mfma_f32_32x32x16_f16 v[32:47], a[240:243], a[176:179], v[32:47]
	ds_read_b64_tr_b16 v[114:115], v210 offset:0x2e00
	ds_read_b64_tr_b16 v[108:109], v210 offset:0x3000
	v_cvt_pk_f16_f32 v119, v240, v241
	v_add_f32_e32 v96, v96, v240
	v_add_f32_e32 v97, v97, v241
	s_mov_b32 s24, s59
	v_mfma_f32_32x32x16_f16 v[80:95], a[212:215], a[148:151], v[80:95]
	ds_read_b64_tr_b16 v[110:111], v210 offset:0x3800
	v_add_f32_e32 v96, v96, v184
	v_add_f32_e32 v97, v97, v185
	s_mov_b32 s30, s60
	v_mfma_f32_32x32x16_f16 v[64:79], a[212:215], a[180:183], v[64:79]
	ds_read_b64_tr_b16 v[104:105], v210 offset:0x3200
	v_add_f32_e32 v96, v96, v186
	v_add_f32_e32 v97, v97, v187
	s_mov_b32 s31, s61
	v_mfma_f32_32x32x16_f16 v[48:63], a[244:247], a[148:151], v[48:63]
	ds_read_b64_tr_b16 v[106:107], v210 offset:0x3a00
	v_add_f32_e32 v96, v96, v188
	v_add_f32_e32 v97, v97, v189
	s_mov_b32 s34, s62
	v_mfma_f32_32x32x16_f16 v[32:47], a[244:247], a[180:183], v[32:47]
	ds_read_b64_tr_b16 v[100:101], v210 offset:0x3400
	ds_read_b64_tr_b16 v[102:103], v210 offset:0x3c00
	v_add_f32_e32 v196, v96, v190
	v_add_f32_e32 v197, v97, v191
	s_mov_b32 s35, s38
	v_mfma_f32_32x32x16_f16 v[80:95], a[216:219], a[152:155], v[80:95]
	ds_read_b64_tr_b16 v[96:97], v210 offset:0x3600
	v_cvt_pk_f16_f32 v140, v141, v142
	v_add_f32_e32 v231, v236, v141
	v_add_f32_e32 v142, v237, v142
	s_mov_b32 s91, s40
	v_mfma_f32_32x32x16_f16 v[64:79], a[216:219], a[184:187], v[64:79]
	ds_read_b64_tr_b16 v[98:99], v210 offset:0x3e00
	v_cvt_pk_f16_f32 v141, v143, v242
	v_add_f32_e32 v143, v231, v143
	v_add_f32_e32 v231, v142, v242
	v_mfma_f32_32x32x16_f16 v[48:63], a[248:251], a[152:155], v[48:63]
	s_mov_b32 s92, s63
	v_cvt_pk_f16_f32 v142, v243, v244
	v_add_f32_e32 v234, v143, v243
	v_add_f32_e32 v231, v231, v244
	v_mfma_f32_32x32x16_f16 v[32:47], a[248:251], a[184:187], v[32:47]
	s_mov_b32 s93, s64
	v_cvt_pk_f16_f32 v143, v245, v246
	v_add_f32_e32 v234, v234, v245
	v_add_f32_e32 v231, v231, v246
	v_mfma_f32_32x32x16_f16 v[80:95], a[220:223], a[156:159], v[80:95]
	s_mov_b32 s94, s65
	v_add_f32_e32 v234, v234, v192
	v_add_f32_e32 v231, v231, v193
	v_mfma_f32_32x32x16_f16 v[64:79], a[220:223], a[188:191], v[64:79]
	s_mov_b32 s95, s44
	v_add_f32_e32 v234, v234, v194
	v_add_f32_e32 v231, v231, v195
	v_mfma_f32_32x32x16_f16 v[48:63], a[252:255], a[156:159], v[48:63]
	s_mov_b32 s96, s66
	v_add_f32_e32 v234, v234, v198
	v_add_f32_e32 v231, v231, v199
	v_mfma_f32_32x32x16_f16 v[32:47], a[252:255], a[188:191], v[32:47]
	s_mov_b32 s97, s67
	v_add_f32_e32 v234, v234, v232
	v_add_f32_e32 v231, v231, v233
	s_nop 0
	s_nop 4
	v_add_f32_e32 v196, v196, v197
	s_waitcnt vmcnt(0) lgkmcnt(0)
	s_barrier
	s_nop 0
	v_mov_b32_e32 v197, v196
	s_nop 1
	v_permlane32_swap_b32_e32 v196, v197
	v_add_f32_e32 v196, v196, v197
	s_nop 0
	v_add_f32_e32 v197, v201, v196
	v_add_f32_e32 v196, v234, v231
	s_nop 0
	v_mov_b32_e32 v231, v196
	s_nop 1
	v_permlane32_swap_b32_e32 v196, v231
	v_add_f32_e32 v196, v196, v231
	s_nop 0
	v_add_f32_e32 v196, v201, v196
	s_nop 1
	s_mov_b32 m0, s0
	v_mfma_f32_32x32x16_f16 a[0:15], v[168:171], v[152:155], 0
	buffer_load_dwordx4 v211, s[16:19], s1 offen lds
	s_nop 0
	s_mov_b32 m0, s12
	v_mfma_f32_32x32x16_f16 a[16:31], v[168:171], v[180:183], 0
	buffer_load_dwordx4 v212, s[16:19], s13 offen lds
	ds_read_b128 a[192:195], v206 offset:0
	s_nop 0
	s_mov_b32 m0, s24
	v_mfma_f32_32x32x16_f16 a[32:47], v[172:175], v[152:155], 0
	buffer_load_dwordx4 v211, s[16:19], s30 offen lds
	ds_read_b128 a[196:199], v207 offset:0
	s_nop 0
	s_mov_b32 m0, s31
	v_mfma_f32_32x32x16_f16 a[48:63], v[172:175], v[180:183], 0
	buffer_load_dwordx4 v212, s[16:19], s34 offen lds
	ds_read_b128 a[200:203], v208 offset:0
	s_nop 0
	s_mov_b32 m0, s35
	v_mfma_f32_32x32x16_f16 a[64:79], v[164:167], v[152:155], 0
	buffer_load_dwordx4 v213, s[20:23], s91 offen lds
	ds_read_b128 a[204:207], v209 offset:0
	s_nop 0
	s_mov_b32 m0, s92
	v_mfma_f32_32x32x16_f16 a[80:95], v[164:167], v[180:183], 0
	buffer_load_dwordx4 v213, s[20:23], s93 offen lds
	ds_read_b128 a[208:211], v206 offset:128
	s_nop 0
	s_mov_b32 m0, s94
	v_mfma_f32_32x32x16_f16 a[96:111], v[176:179], v[152:155], 0
	buffer_load_dwordx4 v213, s[20:23], s95 offen lds
	ds_read_b128 a[212:215], v207 offset:128
	s_nop 0
	s_mov_b32 m0, s96
	v_mfma_f32_32x32x16_f16 a[112:127], v[176:179], v[180:183], 0
	buffer_load_dwordx4 v213, s[20:23], s97 offen lds
	ds_read_b128 a[216:219], v208 offset:128
	s_nop 0
	v_mfma_f32_32x32x16_f16 a[0:15], v[160:163], v[128:131], a[0:15]
	ds_read_b128 a[220:223], v209 offset:128
	v_max3_f32 v152, v80, v81, v48
	v_max3_f32 v153, v82, v83, v49
	s_nop 0
	v_max3_f32 v152, v152, v50, v51
	v_mfma_f32_32x32x16_f16 a[16:31], v[160:163], v[144:147], a[16:31]
	ds_read_b128 a[224:227], v206 offset:8192
	s_nop 0
	v_max3_f32 v152, v152, v84, v85
	v_max3_f32 v153, v153, v86, v87
	s_nop 0
	v_max3_f32 v152, v152, v52, v53
	v_max3_f32 v153, v153, v54, v55
	v_mfma_f32_32x32x16_f16 a[32:47], v[156:159], v[128:131], a[32:47]
	ds_read_b128 a[228:231], v207 offset:8192
	s_nop 0
	v_max3_f32 v152, v152, v88, v89
	v_max3_f32 v153, v153, v90, v91
	s_nop 0
	v_max3_f32 v152, v152, v56, v57
	v_max3_f32 v153, v153, v58, v59
	v_mfma_f32_32x32x16_f16 a[48:63], v[156:159], v[144:147], a[48:63]
	ds_read_b128 a[232:235], v208 offset:8192
	s_nop 0
	v_max3_f32 v152, v152, v92, v93
	v_max3_f32 v153, v153, v94, v95
	s_nop 0
	v_max3_f32 v152, v152, v60, v61
	v_max3_f32 v153, v153, v62, v63
	v_mfma_f32_32x32x16_f16 a[64:79], v[148:151], v[128:131], a[64:79]
	ds_read_b128 a[236:239], v209 offset:8192
	v_max3_f32 v154, v64, v65, v32
	v_max3_f32 v155, v66, v67, v33
	s_nop 0
	v_max3_f32 v154, v154, v34, v35
	v_mfma_f32_32x32x16_f16 a[80:95], v[148:151], v[144:147], a[80:95]
	ds_read_b128 a[240:243], v206 offset:8320
	s_nop 0
	v_max3_f32 v148, v154, v68, v69
	v_max3_f32 v149, v155, v70, v71
	s_nop 0
	v_max3_f32 v148, v148, v36, v37
	v_max3_f32 v149, v149, v38, v39
	v_mfma_f32_32x32x16_f16 a[96:111], v[136:139], v[128:131], a[96:111]
	ds_read_b128 a[244:247], v207 offset:8320
	s_nop 0
	v_max3_f32 v128, v148, v72, v73
	v_max3_f32 v129, v149, v74, v75
	s_nop 0
	v_max3_f32 v128, v128, v40, v41
	v_max3_f32 v129, v129, v42, v43
	v_mfma_f32_32x32x16_f16 a[112:127], v[136:139], v[144:147], a[112:127]
	ds_read_b128 a[248:251], v208 offset:8320
	s_nop 0
	v_max3_f32 v128, v128, v76, v77
	v_max3_f32 v129, v129, v78, v79
	s_nop 0
	v_max3_f32 v128, v128, v44, v45
	v_max3_f32 v130, v129, v46, v47
	v_mfma_f32_32x32x16_f16 a[0:15], v[132:135], v[116:119], a[0:15]
	ds_read_b128 a[252:255], v209 offset:8320
	v_max_f32_e32 v129, v152, v153
	s_nop 0
	v_mov_b32_e32 v131, v129
	s_nop 1
	v_permlane32_swap_b32_e32 v129, v131
	v_max_f32_e32 v129, v129, v131
	v_mfma_f32_32x32x16_f16 a[16:31], v[132:135], v[140:143], a[16:31]
	v_max_f32_e32 v128, v128, v130
	s_nop 0
	v_mov_b32_e32 v130, v128
	s_nop 1
	v_permlane32_swap_b32_e32 v128, v130
	v_max_f32_e32 v128, v128, v130
	v_max_f32_e32 v130, v129, v128
	v_mfma_f32_32x32x16_f16 a[32:47], v[124:127], v[116:119], a[32:47]
	v_cmp_lt_f32_e32 vcc, s79, v130
	s_cmp_lg_u64 vcc, 0
	s_cselect_b64 s[0:1], -1, 0
	s_cbranch_vccnz .LBB3_26
	v_mov_b32_e32 v231, 1.0

.LBB3_12:
	v_exp_f32_e32 v48, v48
	v_exp_f32_e32 v49, v49
	v_mfma_f32_32x32x16_f16 v[112:127], a[192:195], a[128:131], v[16:31]
	ds_read_b64_tr_b16 v[180:181], v225 offset:0
	v_cvt_pk_f16_f32 v164, v128, v129
	v_exp_f32_e32 v50, v50
	v_exp_f32_e32 v51, v51
	v_mfma_f32_32x32x16_f16 v[96:111], a[192:195], a[160:163], v[0:15]
	ds_read_b64_tr_b16 v[182:183], v225 offset:0x800
	v_cvt_pk_f16_f32 v165, v130, v131
	v_mfma_f32_32x32x16_f16 v[80:95], a[224:227], a[128:131], v[16:31]
	ds_read_b64_tr_b16 v[184:185], v225 offset:0x200
	v_exp_f32_e32 v238, v52
	v_exp_f32_e32 v239, v53
	v_cvt_pk_f16_f32 v166, v132, v133
	v_mfma_f32_32x32x16_f16 v[64:79], a[224:227], a[160:163], v[0:15]
	ds_read_b64_tr_b16 v[186:187], v225 offset:0xa00
	ds_read_b64_tr_b16 v[176:177], v225 offset:0x400
	v_exp_f32_e32 v244, v54
	v_exp_f32_e32 v245, v55
	v_cvt_pk_f16_f32 v167, v134, v135
	v_exp_f32_e32 v198, v56
	v_exp_f32_e32 v199, v57
	v_mfma_f32_32x32x16_f16 v[112:127], a[196:199], a[132:135], v[112:127]
	ds_read_b64_tr_b16 v[178:179], v225 offset:0xc00
	v_cvt_pk_f16_f32 v128, v136, v137
	v_exp_f32_e32 v232, v58
	v_exp_f32_e32 v233, v59
	v_mfma_f32_32x32x16_f16 v[96:111], a[196:199], a[164:167], v[96:111]
	ds_read_b64_tr_b16 v[188:189], v225 offset:0x600
	v_cvt_pk_f16_f32 v129, v138, v139
	v_exp_f32_e32 v234, v60
	v_exp_f32_e32 v235, v61
	v_mfma_f32_32x32x16_f16 v[80:95], a[228:231], a[132:135], v[80:95]
	ds_read_b64_tr_b16 v[190:191], v225 offset:0xe00
	v_cvt_pk_f16_f32 v130, v140, v141
	v_mfma_f32_32x32x16_f16 v[64:79], a[228:231], a[164:167], v[64:79]
	ds_read_b64_tr_b16 v[172:173], v225 offset:0x1000
	v_exp_f32_e32 v236, v62
	v_exp_f32_e32 v237, v63
	ds_read_b64_tr_b16 v[174:175], v225 offset:0x1800
	v_cvt_pk_f16_f32 v131, v142, v143
	v_exp_f32_e32 v141, v32
	v_exp_f32_e32 v142, v33
	v_mfma_f32_32x32x16_f16 v[112:127], a[200:203], a[136:139], v[112:127]
	ds_read_b64_tr_b16 v[168:169], v225 offset:0x1200
	v_cvt_pk_f16_f32 v192, v144, v145
	v_exp_f32_e32 v143, v34
	v_mfma_f32_32x32x16_f16 v[96:111], a[200:203], a[168:171], v[96:111]
	ds_read_b64_tr_b16 v[170:171], v225 offset:0x1a00
	v_exp_f32_e32 v246, v35
	v_cvt_pk_f16_f32 v193, v146, v147
	v_mfma_f32_32x32x16_f16 v[80:95], a[232:235], a[136:139], v[80:95]
	ds_read_b64_tr_b16 v[160:161], v225 offset:0x1400
	v_exp_f32_e32 v247, v36
	v_exp_f32_e32 v248, v37
	v_cvt_pk_f16_f32 v194, v148, v149
	v_mfma_f32_32x32x16_f16 v[64:79], a[232:235], a[168:171], v[64:79]
	ds_read_b64_tr_b16 v[162:163], v225 offset:0x1c00
	ds_read_b64_tr_b16 v[136:137], v225 offset:0x1600
	v_exp_f32_e32 v249, v38
	v_exp_f32_e32 v250, v39
	v_cvt_pk_f16_f32 v195, v150, v151
	v_exp_f32_e32 v148, v40
	v_exp_f32_e32 v149, v41
	v_mfma_f32_32x32x16_f16 v[112:127], a[204:207], a[140:143], v[112:127]
	ds_read_b64_tr_b16 v[138:139], v225 offset:0x1e00
	v_cvt_pk_f16_f32 v144, v152, v153
	v_exp_f32_e32 v150, v42
	v_exp_f32_e32 v151, v43
	v_mfma_f32_32x32x16_f16 v[96:111], a[204:207], a[172:175], v[96:111]
	ds_read_b64_tr_b16 v[132:133], v225 offset:0x2000
	v_cvt_pk_f16_f32 v145, v154, v155
	v_exp_f32_e32 v152, v44
	v_exp_f32_e32 v153, v45
	v_mfma_f32_32x32x16_f16 v[80:95], a[236:239], a[140:143], v[80:95]
	ds_read_b64_tr_b16 v[134:135], v225 offset:0x2800
	v_cvt_pk_f16_f32 v146, v156, v157
	v_mfma_f32_32x32x16_f16 v[64:79], a[236:239], a[172:175], v[64:79]
	ds_read_b64_tr_b16 v[60:61], v225 offset:0x2200
	v_exp_f32_e32 v154, v46
	v_exp_f32_e32 v155, v47
	ds_read_b64_tr_b16 v[62:63], v225 offset:0x2a00
	v_cvt_pk_f16_f32 v147, v158, v159
	s_mov_b32 s0, s33
	v_mfma_f32_32x32x16_f16 v[112:127], a[208:211], a[144:147], v[112:127]
	ds_read_b64_tr_b16 v[56:57], v225 offset:0x2400
	v_cvt_pk_f16_f32 v52, v48, v49
	v_add_f32_e32 v32, v241, v48
	v_add_f32_e32 v33, v240, v49
	s_add_i32 s31, s36, s12
	s_add_i32 s24, s31, 0x10000
	s_mov_b32 s1, s24
	v_mfma_f32_32x32x16_f16 v[96:111], a[208:211], a[176:179], v[96:111]
	ds_read_b64_tr_b16 v[58:59], v225 offset:0x2c00
	v_cvt_pk_f16_f32 v53, v50, v51
	v_add_f32_e32 v32, v32, v50
	v_add_f32_e32 v33, v33, v51
	s_mov_b32 s34, s41
	v_mfma_f32_32x32x16_f16 v[80:95], a[240:243], a[144:147], v[80:95]
	ds_read_b64_tr_b16 v[48:49], v225 offset:0x2600
	v_cvt_pk_f16_f32 v54, v238, v239
	v_add_f32_e32 v32, v32, v238
	v_add_f32_e32 v33, v33, v239
	s_add_i32 s35, s31, 0x10400
	v_mfma_f32_32x32x16_f16 v[64:79], a[240:243], a[176:179], v[64:79]
	ds_read_b64_tr_b16 v[50:51], v225 offset:0x2e00
	ds_read_b64_tr_b16 v[44:45], v225 offset:0x3000
	v_cvt_pk_f16_f32 v55, v244, v245
	v_add_f32_e32 v32, v32, v244
	v_add_f32_e32 v33, v33, v245
	s_mov_b32 s91, s43
	v_mfma_f32_32x32x16_f16 v[112:127], a[212:215], a[148:151], v[112:127]
	ds_read_b64_tr_b16 v[46:47], v225 offset:0x3800
	v_add_f32_e32 v32, v32, v198
	v_add_f32_e32 v33, v33, v199
	s_add_i32 s30, s31, 0x10800
	s_mov_b32 s92, s30
	v_mfma_f32_32x32x16_f16 v[96:111], a[212:215], a[180:183], v[96:111]
	ds_read_b64_tr_b16 v[40:41], v225 offset:0x3200
	v_add_f32_e32 v32, v32, v232
	v_add_f32_e32 v33, v33, v233
	s_mov_b32 s93, s45
	v_mfma_f32_32x32x16_f16 v[80:95], a[244:247], a[148:151], v[80:95]
	ds_read_b64_tr_b16 v[42:43], v225 offset:0x3a00
	v_add_f32_e32 v32, v32, v234
	v_add_f32_e32 v33, v33, v235
	s_add_i32 s94, s31, 0x10c00
	v_mfma_f32_32x32x16_f16 v[64:79], a[244:247], a[180:183], v[64:79]
	ds_read_b64_tr_b16 v[36:37], v225 offset:0x3400
	ds_read_b64_tr_b16 v[38:39], v225 offset:0x3c00
	v_add_f32_e32 v156, v32, v236
	v_add_f32_e32 v157, v33, v237
	s_mov_b32 s95, s47
	v_mfma_f32_32x32x16_f16 v[112:127], a[216:219], a[152:155], v[112:127]
	ds_read_b64_tr_b16 v[32:33], v225 offset:0x3600
	v_cvt_pk_f16_f32 v140, v141, v142
	v_add_f32_e32 v158, v242, v141
	v_add_f32_e32 v142, v243, v142
	s_add_i32 s96, s31, 0xc000
	v_mfma_f32_32x32x16_f16 v[96:111], a[216:219], a[184:187], v[96:111]
	ds_read_b64_tr_b16 v[34:35], v225 offset:0x3e00
	v_cvt_pk_f16_f32 v141, v143, v246
	v_add_f32_e32 v143, v158, v143
	v_add_f32_e32 v158, v142, v246
	v_mfma_f32_32x32x16_f16 v[80:95], a[248:251], a[152:155], v[80:95]
	s_mov_b32 s97, s49
	v_cvt_pk_f16_f32 v142, v247, v248
	v_add_f32_e32 v159, v143, v247
	v_add_f32_e32 v158, v158, v248
	v_mfma_f32_32x32x16_f16 v[64:79], a[248:251], a[184:187], v[64:79]
	s_add_i32 s98, s31, 0xc080
	v_cvt_pk_f16_f32 v143, v249, v250
	v_add_f32_e32 v159, v159, v249
	v_add_f32_e32 v158, v158, v250
	v_mfma_f32_32x32x16_f16 v[112:127], a[220:223], a[156:159], v[112:127]
	s_mov_b32 s99, s51
	v_add_f32_e32 v159, v159, v148
	v_add_f32_e32 v158, v158, v149
	v_mfma_f32_32x32x16_f16 v[96:111], a[220:223], a[188:191], v[96:111]
	s_add_i32 vcc_lo, s31, 0xc800
	v_add_f32_e32 v159, v159, v150
	v_add_f32_e32 v158, v158, v151
	v_mfma_f32_32x32x16_f16 v[80:95], a[252:255], a[156:159], v[80:95]
	s_mov_b32 vcc_hi, s53
	v_add_f32_e32 v159, v159, v152
	v_add_f32_e32 v158, v158, v153
	v_mfma_f32_32x32x16_f16 v[64:79], a[252:255], a[188:191], v[64:79]
	s_add_i32 s80, s31, 0xc880
	v_add_f32_e32 v159, v159, v154
	v_add_f32_e32 v158, v158, v155
	s_nop 4
	v_add_f32_e32 v156, v156, v157
	s_waitcnt vmcnt(0) lgkmcnt(0)
	s_barrier
	v_mov_b32_e32 v157, v156
	s_nop 1
	v_permlane32_swap_b32_e32 v156, v157
	v_add_f32_e32 v156, v156, v157
	v_add_f32_e32 v197, v197, v156
	v_add_f32_e32 v156, v159, v158
	v_mov_b32_e32 v157, v156
	s_nop 1
	v_permlane32_swap_b32_e32 v156, v157
	v_add_f32_e32 v156, v156, v157
	v_add_f32_e32 v196, v196, v156
	s_nop 1
	s_mov_b32 m0, s0
	v_mfma_f32_32x32x16_f16 a[0:15], v[180:183], v[164:167], a[0:15]
	buffer_load_dwordx4 v211, s[16:19], s1 offen lds
	s_mov_b32 m0, s34
	v_mfma_f32_32x32x16_f16 a[16:31], v[180:183], v[192:195], a[16:31]
	buffer_load_dwordx4 v212, s[16:19], s35 offen lds
	ds_read_b128 a[192:195], v221 offset:0
	s_mov_b32 m0, s91
	v_mfma_f32_32x32x16_f16 a[32:47], v[184:187], v[164:167], a[32:47]
	buffer_load_dwordx4 v211, s[16:19], s92 offen lds
	ds_read_b128 a[196:199], v222 offset:0
	s_mov_b32 m0, s93
	v_mfma_f32_32x32x16_f16 a[48:63], v[184:187], v[192:195], a[48:63]
	buffer_load_dwordx4 v212, s[16:19], s94 offen lds
	ds_read_b128 a[200:203], v223 offset:0
	s_mov_b32 m0, s95
	v_mfma_f32_32x32x16_f16 a[64:79], v[176:179], v[164:167], a[64:79]
	buffer_load_dwordx4 v213, s[20:23], s96 offen lds
	ds_read_b128 a[204:207], v224 offset:0
	s_mov_b32 m0, s97
	v_mfma_f32_32x32x16_f16 a[80:95], v[176:179], v[192:195], a[80:95]
	buffer_load_dwordx4 v213, s[20:23], s98 offen lds
	ds_read_b128 a[208:211], v221 offset:128
	s_mov_b32 m0, s99
	v_mfma_f32_32x32x16_f16 a[96:111], v[188:191], v[164:167], a[96:111]
	buffer_load_dwordx4 v213, s[20:23], vcc_lo offen lds
	ds_read_b128 a[212:215], v222 offset:128
	s_mov_b32 m0, vcc_hi
	v_mfma_f32_32x32x16_f16 a[112:127], v[188:191], v[192:195], a[112:127]
	buffer_load_dwordx4 v213, s[20:23], s80 offen lds
	ds_read_b128 a[216:219], v223 offset:128
	v_mfma_f32_32x32x16_f16 a[0:15], v[172:175], v[128:131], a[0:15]
	ds_read_b128 a[220:223], v224 offset:128
	v_max3_f32 v156, v112, v113, v80
	v_max3_f32 v157, v114, v115, v81
	v_max3_f32 v156, v156, v82, v83
	v_mfma_f32_32x32x16_f16 a[16:31], v[172:175], v[144:147], a[16:31]
	ds_read_b128 a[224:227], v221 offset:8192
	v_max3_f32 v156, v156, v116, v117
	v_max3_f32 v157, v157, v118, v119
	v_max3_f32 v156, v156, v84, v85
	v_max3_f32 v157, v157, v86, v87
	v_mfma_f32_32x32x16_f16 a[32:47], v[168:171], v[128:131], a[32:47]
	ds_read_b128 a[228:231], v222 offset:8192
	v_max3_f32 v156, v156, v120, v121
	v_max3_f32 v157, v157, v122, v123
	v_max3_f32 v156, v156, v88, v89
	v_max3_f32 v157, v157, v90, v91
	v_mfma_f32_32x32x16_f16 a[48:63], v[168:171], v[144:147], a[48:63]
	ds_read_b128 a[232:235], v223 offset:8192
	v_max3_f32 v156, v156, v124, v125
	v_max3_f32 v157, v157, v126, v127
	v_max3_f32 v156, v156, v92, v93
	v_max3_f32 v157, v157, v94, v95
	v_mfma_f32_32x32x16_f16 a[64:79], v[160:163], v[128:131], a[64:79]
	ds_read_b128 a[236:239], v224 offset:8192
	v_max3_f32 v158, v96, v97, v64
	v_max3_f32 v159, v98, v99, v65
	v_max3_f32 v158, v158, v66, v67
	v_mfma_f32_32x32x16_f16 a[80:95], v[160:163], v[144:147], a[80:95]
	ds_read_b128 a[240:243], v221 offset:8320
	v_max3_f32 v158, v158, v100, v101
	v_max3_f32 v159, v159, v102, v103
	v_max3_f32 v158, v158, v68, v69
	v_max3_f32 v159, v159, v70, v71
	v_mfma_f32_32x32x16_f16 a[96:111], v[136:139], v[128:131], a[96:111]
	ds_read_b128 a[244:247], v222 offset:8320
	v_max3_f32 v128, v158, v104, v105
	v_max3_f32 v129, v159, v106, v107
	v_max3_f32 v128, v128, v72, v73
	v_max3_f32 v129, v129, v74, v75
	v_mfma_f32_32x32x16_f16 a[112:127], v[136:139], v[144:147], a[112:127]
	ds_read_b128 a[248:251], v223 offset:8320
	v_max3_f32 v128, v128, v108, v109
	v_max3_f32 v129, v129, v110, v111
	v_max3_f32 v128, v128, v76, v77
	v_max3_f32 v130, v129, v78, v79
	v_mfma_f32_32x32x16_f16 a[0:15], v[132:135], v[52:55], a[0:15]
	ds_read_b128 a[252:255], v224 offset:8320
	v_max_f32_e32 v129, v156, v157
	v_mov_b32_e32 v131, v129
	s_nop 1
	v_permlane32_swap_b32_e32 v129, v131
	v_max_f32_e32 v129, v129, v131
	v_mfma_f32_32x32x16_f16 a[16:31], v[132:135], v[140:143], a[16:31]
	v_max_f32_e32 v128, v128, v130
	v_mov_b32_e32 v130, v128
	s_nop 1
	v_permlane32_swap_b32_e32 v128, v130
	v_max_f32_e32 v128, v128, v130
	v_max_f32_e32 v130, v129, v128
	v_mfma_f32_32x32x16_f16 a[32:47], v[60:63], v[52:55], a[32:47]
	v_cmp_lt_f32_e32 vcc, s79, v130
	s_cmp_lg_u64 vcc, 0
	s_cselect_b64 s[0:1], -1, 0
	s_cbranch_vccnz .LBB3_17

.LBB3_14:
	s_waitcnt lgkmcnt(0)
	v_exp_f32_e32 v80, v80
	v_exp_f32_e32 v81, v81
	v_mfma_f32_32x32x16_f16 v[112:127], a[192:195], a[128:131], v[16:31]
	ds_read_b64_tr_b16 v[180:181], v210 offset:0
	v_cvt_pk_f16_f32 v164, v128, v129
	v_exp_f32_e32 v82, v82
	v_exp_f32_e32 v83, v83
	v_mfma_f32_32x32x16_f16 v[96:111], a[192:195], a[160:163], v[0:15]
	ds_read_b64_tr_b16 v[182:183], v210 offset:0x800
	v_cvt_pk_f16_f32 v165, v130, v131
	v_mfma_f32_32x32x16_f16 v[48:63], a[224:227], a[128:131], v[16:31]
	ds_read_b64_tr_b16 v[184:185], v210 offset:0x200
	v_exp_f32_e32 v242, v84
	v_exp_f32_e32 v243, v85
	v_cvt_pk_f16_f32 v166, v132, v133
	v_mfma_f32_32x32x16_f16 v[32:47], a[224:227], a[160:163], v[0:15]
	ds_read_b64_tr_b16 v[186:187], v210 offset:0xa00
	ds_read_b64_tr_b16 v[176:177], v210 offset:0x400
	v_exp_f32_e32 v244, v86
	v_exp_f32_e32 v245, v87
	v_cvt_pk_f16_f32 v167, v134, v135
	v_exp_f32_e32 v198, v88
	v_exp_f32_e32 v199, v89
	v_mfma_f32_32x32x16_f16 v[112:127], a[196:199], a[132:135], v[112:127]
	ds_read_b64_tr_b16 v[178:179], v210 offset:0xc00
	v_cvt_pk_f16_f32 v128, v136, v137
	v_exp_f32_e32 v232, v90
	v_exp_f32_e32 v233, v91
	v_mfma_f32_32x32x16_f16 v[96:111], a[196:199], a[164:167], v[96:111]
	ds_read_b64_tr_b16 v[188:189], v210 offset:0x600
	v_cvt_pk_f16_f32 v129, v138, v139
	v_exp_f32_e32 v234, v92
	v_exp_f32_e32 v235, v93
	v_mfma_f32_32x32x16_f16 v[48:63], a[228:231], a[132:135], v[48:63]
	ds_read_b64_tr_b16 v[190:191], v210 offset:0xe00
	v_cvt_pk_f16_f32 v130, v140, v141
	v_mfma_f32_32x32x16_f16 v[32:47], a[228:231], a[164:167], v[32:47]
	ds_read_b64_tr_b16 v[172:173], v210 offset:0x1000
	v_exp_f32_e32 v236, v94
	v_exp_f32_e32 v237, v95
	ds_read_b64_tr_b16 v[174:175], v210 offset:0x1800
	v_cvt_pk_f16_f32 v131, v142, v143
	v_exp_f32_e32 v141, v64
	v_exp_f32_e32 v142, v65
	v_mfma_f32_32x32x16_f16 v[112:127], a[200:203], a[136:139], v[112:127]
	ds_read_b64_tr_b16 v[168:169], v210 offset:0x1200
	v_cvt_pk_f16_f32 v192, v144, v145
	v_exp_f32_e32 v143, v66
	v_mfma_f32_32x32x16_f16 v[96:111], a[200:203], a[168:171], v[96:111]
	ds_read_b64_tr_b16 v[170:171], v210 offset:0x1a00
	v_exp_f32_e32 v246, v67
	v_cvt_pk_f16_f32 v193, v146, v147
	v_mfma_f32_32x32x16_f16 v[48:63], a[232:235], a[136:139], v[48:63]
	ds_read_b64_tr_b16 v[160:161], v210 offset:0x1400
	v_exp_f32_e32 v247, v68
	v_exp_f32_e32 v248, v69
	v_cvt_pk_f16_f32 v194, v148, v149
	v_mfma_f32_32x32x16_f16 v[32:47], a[232:235], a[168:171], v[32:47]
	ds_read_b64_tr_b16 v[162:163], v210 offset:0x1c00
	ds_read_b64_tr_b16 v[136:137], v210 offset:0x1600
	v_exp_f32_e32 v249, v70
	v_exp_f32_e32 v250, v71
	v_cvt_pk_f16_f32 v195, v150, v151
	v_exp_f32_e32 v148, v72
	v_exp_f32_e32 v149, v73
	v_mfma_f32_32x32x16_f16 v[112:127], a[204:207], a[140:143], v[112:127]
	ds_read_b64_tr_b16 v[138:139], v210 offset:0x1e00
	v_cvt_pk_f16_f32 v144, v152, v153
	v_exp_f32_e32 v150, v74
	v_exp_f32_e32 v151, v75
	v_mfma_f32_32x32x16_f16 v[96:111], a[204:207], a[172:175], v[96:111]
	ds_read_b64_tr_b16 v[132:133], v210 offset:0x2000
	v_cvt_pk_f16_f32 v145, v154, v155
	v_exp_f32_e32 v152, v76
	v_exp_f32_e32 v153, v77
	v_mfma_f32_32x32x16_f16 v[48:63], a[236:239], a[140:143], v[48:63]
	ds_read_b64_tr_b16 v[134:135], v210 offset:0x2800
	v_cvt_pk_f16_f32 v146, v156, v157
	v_mfma_f32_32x32x16_f16 v[32:47], a[236:239], a[172:175], v[32:47]
	ds_read_b64_tr_b16 v[92:93], v210 offset:0x2200
	v_exp_f32_e32 v154, v78
	v_exp_f32_e32 v155, v79
	ds_read_b64_tr_b16 v[94:95], v210 offset:0x2a00
	v_cvt_pk_f16_f32 v147, v158, v159
	s_mov_b32 s0, s55
	v_mfma_f32_32x32x16_f16 v[112:127], a[208:211], a[144:147], v[112:127]
	ds_read_b64_tr_b16 v[88:89], v210 offset:0x2400
	v_cvt_pk_f16_f32 v84, v80, v81
	v_add_f32_e32 v64, v239, v80
	v_add_f32_e32 v65, v238, v81
	s_add_i32 s1, s31, 0x14000
	v_mfma_f32_32x32x16_f16 v[96:111], a[208:211], a[176:179], v[96:111]
	ds_read_b64_tr_b16 v[90:91], v210 offset:0x2c00
	v_cvt_pk_f16_f32 v85, v82, v83
	v_add_f32_e32 v64, v64, v82
	v_add_f32_e32 v65, v65, v83
	s_mov_b32 s34, s57
	v_mfma_f32_32x32x16_f16 v[48:63], a[240:243], a[144:147], v[48:63]
	ds_read_b64_tr_b16 v[80:81], v210 offset:0x2600
	v_cvt_pk_f16_f32 v86, v242, v243
	v_add_f32_e32 v64, v64, v242
	v_add_f32_e32 v65, v65, v243
	s_add_i32 s35, s31, 0x14400
	v_mfma_f32_32x32x16_f16 v[32:47], a[240:243], a[176:179], v[32:47]
	ds_read_b64_tr_b16 v[82:83], v210 offset:0x2e00
	ds_read_b64_tr_b16 v[76:77], v210 offset:0x3000
	v_cvt_pk_f16_f32 v87, v244, v245
	v_add_f32_e32 v64, v64, v244
	v_add_f32_e32 v65, v65, v245
	s_mov_b32 s91, s59
	v_mfma_f32_32x32x16_f16 v[112:127], a[212:215], a[148:151], v[112:127]
	ds_read_b64_tr_b16 v[78:79], v210 offset:0x3800
	v_add_f32_e32 v64, v64, v198
	v_add_f32_e32 v65, v65, v199
	s_add_i32 s92, s31, 0x14800
	v_mfma_f32_32x32x16_f16 v[96:111], a[212:215], a[180:183], v[96:111]
	ds_read_b64_tr_b16 v[72:73], v210 offset:0x3200
	v_add_f32_e32 v64, v64, v232
	v_add_f32_e32 v65, v65, v233
	s_mov_b32 s93, s61
	v_mfma_f32_32x32x16_f16 v[48:63], a[244:247], a[148:151], v[48:63]
	ds_read_b64_tr_b16 v[74:75], v210 offset:0x3a00
	v_add_f32_e32 v64, v64, v234
	v_add_f32_e32 v65, v65, v235
	s_add_i32 s94, s31, 0x14c00
	v_mfma_f32_32x32x16_f16 v[32:47], a[244:247], a[180:183], v[32:47]
	ds_read_b64_tr_b16 v[68:69], v210 offset:0x3400
	ds_read_b64_tr_b16 v[70:71], v210 offset:0x3c00
	v_add_f32_e32 v156, v64, v236
	v_add_f32_e32 v157, v65, v237
	s_mov_b32 s95, s38
	v_mfma_f32_32x32x16_f16 v[112:127], a[216:219], a[152:155], v[112:127]
	ds_read_b64_tr_b16 v[64:65], v210 offset:0x3600
	v_cvt_pk_f16_f32 v140, v141, v142
	v_add_f32_e32 v158, v240, v141
	v_add_f32_e32 v142, v241, v142
	v_mfma_f32_32x32x16_f16 v[96:111], a[216:219], a[184:187], v[96:111]
	ds_read_b64_tr_b16 v[66:67], v210 offset:0x3e00
	v_cvt_pk_f16_f32 v141, v143, v246
	v_add_f32_e32 v143, v158, v143
	v_add_f32_e32 v158, v142, v246
	v_mfma_f32_32x32x16_f16 v[48:63], a[248:251], a[152:155], v[48:63]
	s_mov_b32 s80, s63
	v_cvt_pk_f16_f32 v142, v247, v248
	v_add_f32_e32 v159, v143, v247
	v_add_f32_e32 v158, v158, v248
	v_mfma_f32_32x32x16_f16 v[32:47], a[248:251], a[184:187], v[32:47]
	s_add_i32 s96, s31, 0x10080
	v_cvt_pk_f16_f32 v143, v249, v250
	v_add_f32_e32 v159, v159, v249
	v_add_f32_e32 v158, v158, v250
	v_mfma_f32_32x32x16_f16 v[112:127], a[220:223], a[156:159], v[112:127]
	s_mov_b32 s97, s65
	v_add_f32_e32 v159, v159, v148
	v_add_f32_e32 v158, v158, v149
	v_mfma_f32_32x32x16_f16 v[96:111], a[220:223], a[188:191], v[96:111]
	v_add_f32_e32 v159, v159, v150
	v_add_f32_e32 v158, v158, v151
	v_mfma_f32_32x32x16_f16 v[48:63], a[252:255], a[156:159], v[48:63]
	s_mov_b32 s98, s66
	v_add_f32_e32 v159, v159, v152
	v_add_f32_e32 v158, v158, v153
	v_mfma_f32_32x32x16_f16 v[32:47], a[252:255], a[188:191], v[32:47]
	s_add_i32 s31, s31, 0x10880
	v_add_f32_e32 v159, v159, v154
	v_add_f32_e32 v158, v158, v155
	s_nop 4
	v_add_f32_e32 v156, v156, v157
	s_waitcnt vmcnt(0) lgkmcnt(0)
	s_barrier
	v_mov_b32_e32 v157, v156
	s_nop 1
	v_permlane32_swap_b32_e32 v156, v157
	v_add_f32_e32 v156, v156, v157
	v_add_f32_e32 v197, v197, v156
	v_add_f32_e32 v156, v159, v158
	v_mov_b32_e32 v157, v156
	s_nop 1
	v_permlane32_swap_b32_e32 v156, v157
	v_add_f32_e32 v156, v156, v157
	v_add_f32_e32 v196, v196, v156
	s_nop 1
	s_mov_b32 m0, s0
	v_mfma_f32_32x32x16_f16 a[0:15], v[180:183], v[164:167], a[0:15]
	buffer_load_dwordx4 v211, s[16:19], s1 offen lds
	s_mov_b32 m0, s34
	v_mfma_f32_32x32x16_f16 a[16:31], v[180:183], v[192:195], a[16:31]
	buffer_load_dwordx4 v212, s[16:19], s35 offen lds
	ds_read_b128 a[192:195], v206 offset:0
	s_mov_b32 m0, s91
	v_mfma_f32_32x32x16_f16 a[32:47], v[184:187], v[164:167], a[32:47]
	buffer_load_dwordx4 v211, s[16:19], s92 offen lds
	ds_read_b128 a[196:199], v207 offset:0
	s_mov_b32 m0, s93
	v_mfma_f32_32x32x16_f16 a[48:63], v[184:187], v[192:195], a[48:63]
	buffer_load_dwordx4 v212, s[16:19], s94 offen lds
	ds_read_b128 a[200:203], v208 offset:0
	s_mov_b32 m0, s95
	v_mfma_f32_32x32x16_f16 a[64:79], v[176:179], v[164:167], a[64:79]
	buffer_load_dwordx4 v213, s[20:23], s24 offen lds
	ds_read_b128 a[204:207], v209 offset:0
	s_mov_b32 m0, s80
	v_mfma_f32_32x32x16_f16 a[80:95], v[176:179], v[192:195], a[80:95]
	buffer_load_dwordx4 v213, s[20:23], s96 offen lds
	ds_read_b128 a[208:211], v206 offset:128
	s_mov_b32 m0, s97
	v_mfma_f32_32x32x16_f16 a[96:111], v[188:191], v[164:167], a[96:111]
	buffer_load_dwordx4 v213, s[20:23], s30 offen lds
	ds_read_b128 a[212:215], v207 offset:128
	s_mov_b32 m0, s98
	v_mfma_f32_32x32x16_f16 a[112:127], v[188:191], v[192:195], a[112:127]
	buffer_load_dwordx4 v213, s[20:23], s31 offen lds
	ds_read_b128 a[216:219], v208 offset:128
	v_mfma_f32_32x32x16_f16 a[0:15], v[172:175], v[128:131], a[0:15]
	ds_read_b128 a[220:223], v209 offset:128
	v_max3_f32 v156, v112, v113, v48
	v_max3_f32 v157, v114, v115, v49
	v_max3_f32 v156, v156, v50, v51
	v_mfma_f32_32x32x16_f16 a[16:31], v[172:175], v[144:147], a[16:31]
	ds_read_b128 a[224:227], v206 offset:8192
	v_max3_f32 v156, v156, v116, v117
	v_max3_f32 v157, v157, v118, v119
	v_max3_f32 v156, v156, v52, v53
	v_max3_f32 v157, v157, v54, v55
	v_mfma_f32_32x32x16_f16 a[32:47], v[168:171], v[128:131], a[32:47]
	ds_read_b128 a[228:231], v207 offset:8192
	v_max3_f32 v156, v156, v120, v121
	v_max3_f32 v157, v157, v122, v123
	v_max3_f32 v156, v156, v56, v57
	v_max3_f32 v157, v157, v58, v59
	v_mfma_f32_32x32x16_f16 a[48:63], v[168:171], v[144:147], a[48:63]
	ds_read_b128 a[232:235], v208 offset:8192
	v_max3_f32 v156, v156, v124, v125
	v_max3_f32 v157, v157, v126, v127
	v_max3_f32 v156, v156, v60, v61
	v_max3_f32 v157, v157, v62, v63
	v_mfma_f32_32x32x16_f16 a[64:79], v[160:163], v[128:131], a[64:79]
	ds_read_b128 a[236:239], v209 offset:8192
	v_max3_f32 v158, v96, v97, v32
	v_max3_f32 v159, v98, v99, v33
	v_max3_f32 v158, v158, v34, v35
	v_mfma_f32_32x32x16_f16 a[80:95], v[160:163], v[144:147], a[80:95]
	ds_read_b128 a[240:243], v206 offset:8320
	v_max3_f32 v158, v158, v100, v101
	v_max3_f32 v159, v159, v102, v103
	v_max3_f32 v158, v158, v36, v37
	v_max3_f32 v159, v159, v38, v39
	v_mfma_f32_32x32x16_f16 a[96:111], v[136:139], v[128:131], a[96:111]
	ds_read_b128 a[244:247], v207 offset:8320
	v_max3_f32 v128, v158, v104, v105
	v_max3_f32 v129, v159, v106, v107
	v_max3_f32 v128, v128, v40, v41
	v_max3_f32 v129, v129, v42, v43
	v_mfma_f32_32x32x16_f16 a[112:127], v[136:139], v[144:147], a[112:127]
	ds_read_b128 a[248:251], v208 offset:8320
	v_max3_f32 v128, v128, v108, v109
	v_max3_f32 v129, v129, v110, v111
	v_max3_f32 v128, v128, v44, v45
	v_max3_f32 v130, v129, v46, v47
	v_mfma_f32_32x32x16_f16 a[0:15], v[132:135], v[84:87], a[0:15]
	ds_read_b128 a[252:255], v209 offset:8320
	v_max_f32_e32 v129, v156, v157
	v_mov_b32_e32 v131, v129
	s_nop 1
	v_permlane32_swap_b32_e32 v129, v131
	v_max_f32_e32 v129, v129, v131
	v_mfma_f32_32x32x16_f16 a[16:31], v[132:135], v[140:143], a[16:31]
	v_max_f32_e32 v128, v128, v130
	v_mov_b32_e32 v130, v128
	s_nop 1
	v_permlane32_swap_b32_e32 v128, v130
	v_max_f32_e32 v128, v128, v130
	v_max_f32_e32 v130, v129, v128
	v_mfma_f32_32x32x16_f16 a[32:47], v[92:95], v[84:87], a[32:47]
	v_cmp_lt_f32_e32 vcc, s79, v130
	s_cmp_lg_u64 vcc, 0
	s_cselect_b64 s[0:1], -1, 0
	s_cbranch_vccnz .LBB3_19
